# saddr-form LDS-DMA addressing in GEMM loops + early buffer_inv in grid barriers
# speedup vs baseline: 1.0111x; 1.0111x over previous
; __device__ __forceinline__ unsigned xb_ld(unsigned* p)              { return __hip_atomic_load(p, __ATOMIC_RELAXED, __HIP_MEMORY_SCOPE_AGENT); }
; __device__ __forceinline__ unsigned xb_add(unsigned* p, unsigned v) { return __hip_atomic_fetch_add(p, v, __ATOMIC_RELAXED, __HIP_MEMORY_SCOPE_AGENT); }
; #define XB_SPIN(cond, bar) do { unsigned _sp = 0; while (cond) { __builtin_amdgcn_s_sleep(1); \
;     if ((++_sp & 255u) == 0u) { if (xb_ld(&(bar)[XB_TMO])) break; if (_sp > XB_SPIN_CAP) { atomicAdd(&(bar)[XB_TMO], 1u); break; } } } } while (0)
; __device__ __forceinline__ void xcd_barrier(const XcdBarrier& b) {
;     asm volatile("s_waitcnt vmcnt(0)" ::: "memory");
;     __syncthreads();
;     if (threadIdx.x == 0) {
;         unsigned* bar = b.bar;
;         __builtin_amdgcn_s_waitcnt(0);
;         unsigned nloc = b.st[0], nx = b.st[1];
;         if (nloc == 0u) { xcd_barrier_complete(bar, b.x, nloc, nx); b.st[0] = nloc; b.st[1] = nx; }
;         const unsigned old = xb_add(&bar[XB_XSUB(b.x)], 1u);
;         const unsigned gen = old / nloc;
;         if (old + 1u == (gen + 1u) * nloc) {
;             __builtin_amdgcn_fence(__ATOMIC_RELEASE, "agent");
;             asm volatile("s_waitcnt vmcnt(0)" ::: "memory");
;             const unsigned og = xb_add(&bar[XB_TOP], 1u);
;             const unsigned tg = og / nx;
;             if (og + 1u == (tg + 1u) * nx) xb_add(&bar[XB_TOPGEN], 1u);
;             else XB_SPIN(xb_ld(&bar[XB_TOPGEN]) == tg, bar);
;             __builtin_amdgcn_fence(__ATOMIC_ACQUIRE, "agent");
;             xb_add(&bar[XB_XGEN(b.x)], 1u);
;             asm volatile("s_waitcnt vmcnt(0)" ::: "memory");
;         } else {
;             XB_SPIN(xb_ld(&bar[XB_XGEN(b.x)]) == gen, bar);
.LBB0_290:
	s_or_b64 exec, exec, s[8:9]
	v_cvt_f32_u32_e32 v5, v3
	s_waitcnt vmcnt(0)
	v_readfirstlane_b32 s6, v4
	v_sub_u32_e32 v4, 0, v3
	v_rcp_iflag_f32_e32 v5, v5
	v_add_u32_e32 v6, s6, v2
	v_mul_f32_e32 v5, 0x4f7ffffe, v5
	v_cvt_u32_f32_e32 v5, v5
	v_mul_lo_u32 v2, v4, v5
	v_mul_hi_u32 v2, v5, v2
	v_add_u32_e32 v2, v5, v2
	v_mul_hi_u32 v2, v6, v2
	v_mul_lo_u32 v4, v2, v3
	v_sub_u32_e32 v4, v6, v4
	v_add_u32_e32 v5, 1, v2
	v_cmp_ge_u32_e32 vcc, v4, v3
	s_nop 1
	v_cndmask_b32_e32 v2, v2, v5, vcc
	v_sub_u32_e32 v5, v4, v3
	v_cndmask_b32_e32 v4, v4, v5, vcc
	v_add_u32_e32 v5, 1, v2
	v_cmp_ge_u32_e32 vcc, v4, v3
	v_add_u32_e32 v4, 1, v6
	s_nop 0
	v_cndmask_b32_e32 v2, v2, v5, vcc
	v_mul_lo_u32 v5, v3, v2
	v_add_u32_e32 v3, v5, v3
	v_cmp_ne_u32_e32 vcc, v4, v3
	s_and_saveexec_b64 s[6:7], vcc
	s_xor_b64 s[6:7], exec, s[6:7]
	s_cbranch_execz .LBB0_304
	s_waitcnt lgkmcnt(0)
	buffer_inv sc1
	v_mov_b32_e32 v1, 0x2000
	global_load_dword v1, v1, s[4:5] offset:1024 sc1
	s_add_u32 s12, s4, 0x2400
	s_addc_u32 s13, s5, 0
	s_waitcnt vmcnt(0)
	v_cmp_eq_u32_e32 vcc, v1, v2
	s_and_saveexec_b64 s[8:9], vcc
	s_cbranch_execz .LBB0_303
	v_readlane_b32 s10, v249, 11
	v_readlane_b32 s11, v249, 12
	s_add_u32 s10, s10, 0x4200
	s_addc_u32 s11, s11, 0
	s_mov_b32 s24, 1
	s_mov_b64 s[14:15], 0
	v_mov_b32_e32 v1, 0
	s_branch .LBB0_294

; __device__ __forceinline__ unsigned xb_ld(unsigned* p)              { return __hip_atomic_load(p, __ATOMIC_RELAXED, __HIP_MEMORY_SCOPE_AGENT); }
; __device__ __forceinline__ unsigned xb_add(unsigned* p, unsigned v) { return __hip_atomic_fetch_add(p, v, __ATOMIC_RELAXED, __HIP_MEMORY_SCOPE_AGENT); }
; #define XB_SPIN(cond, bar) do { unsigned _sp = 0; while (cond) { __builtin_amdgcn_s_sleep(1); \
;     if ((++_sp & 255u) == 0u) { if (xb_ld(&(bar)[XB_TMO])) break; if (_sp > XB_SPIN_CAP) { atomicAdd(&(bar)[XB_TMO], 1u); break; } } } } while (0)
; __device__ __forceinline__ void xcd_barrier(const XcdBarrier& b) {
;     ...
;         if (old + 1u == (gen + 1u) * nloc) {
;             __builtin_amdgcn_fence(__ATOMIC_RELEASE, "agent");
;             asm volatile("s_waitcnt vmcnt(0)" ::: "memory");
;             const unsigned og = xb_add(&bar[XB_TOP], 1u);
;             const unsigned tg = og / nx;
;             if (og + 1u == (tg + 1u) * nx) xb_add(&bar[XB_TOPGEN], 1u);
;             else XB_SPIN(xb_ld(&bar[XB_TOPGEN]) == tg, bar);
;             __builtin_amdgcn_fence(__ATOMIC_ACQUIRE, "agent");
;             xb_add(&bar[XB_XGEN(b.x)], 1u);
;             asm volatile("s_waitcnt vmcnt(0)" ::: "memory");
;         } else {
;             XB_SPIN(xb_ld(&bar[XB_XGEN(b.x)]) == gen, bar);
;             __builtin_amdgcn_fence(__ATOMIC_ACQUIRE, "agent");
;             asm volatile("s_waitcnt vmcnt(0)" ::: "memory");
.LBB0_303:
	s_or_b64 exec, exec, s[8:9]
	s_waitcnt vmcnt(0)
	s_waitcnt vmcnt(0)
.LBB0_304:
	s_andn2_saveexec_b64 s[6:7], s[6:7]
	s_cbranch_execz .LBB0_324
	s_mov_b64 s[6:7], exec
	buffer_wbl2 sc1
	s_waitcnt lgkmcnt(0)
	s_waitcnt vmcnt(0)
	buffer_inv sc1
	v_mbcnt_lo_u32_b32 v2, s6, 0
	v_mbcnt_hi_u32_b32 v2, s7, v2
	v_cmp_eq_u32_e32 vcc, 0, v2
	s_and_saveexec_b64 s[8:9], vcc
	s_cbranch_execz .LBB0_307
	s_bcnt1_i32_b64 s6, s[6:7]
	v_mov_b32_e32 v4, s6
	v_readlane_b32 s6, v249, 11
	v_mov_b32_e32 v3, 0x7000
	v_readlane_b32 s7, v249, 12
	s_nop 4
	global_atomic_add v3, v3, v4, s[6:7] offset:1024 sc0

; __device__ __forceinline__ unsigned xb_ld(unsigned* p)              { return __hip_atomic_load(p, __ATOMIC_RELAXED, __HIP_MEMORY_SCOPE_AGENT); }
; __device__ __forceinline__ unsigned xb_add(unsigned* p, unsigned v) { return __hip_atomic_fetch_add(p, v, __ATOMIC_RELAXED, __HIP_MEMORY_SCOPE_AGENT); }
; #define XB_SPIN(cond, bar) do { unsigned _sp = 0; while (cond) { __builtin_amdgcn_s_sleep(1); \
;     if ((++_sp & 255u) == 0u) { if (xb_ld(&(bar)[XB_TMO])) break; if (_sp > XB_SPIN_CAP) { atomicAdd(&(bar)[XB_TMO], 1u); break; } } } } while (0)
; __device__ __forceinline__ void xcd_barrier(const XcdBarrier& b) {
;     ...
;             if (og + 1u == (tg + 1u) * nx) xb_add(&bar[XB_TOPGEN], 1u);
;             else XB_SPIN(xb_ld(&bar[XB_TOPGEN]) == tg, bar);
;             __builtin_amdgcn_fence(__ATOMIC_ACQUIRE, "agent");
;             xb_add(&bar[XB_XGEN(b.x)], 1u);
;             asm volatile("s_waitcnt vmcnt(0)" ::: "memory");
.LBB0_321:
	s_or_b64 exec, exec, s[6:7]
	s_mov_b64 s[6:7], exec
	v_mbcnt_lo_u32_b32 v1, s6, 0
	v_mbcnt_hi_u32_b32 v1, s7, v1
	v_cmp_eq_u32_e32 vcc, 0, v1
	s_waitcnt vmcnt(0)
	s_and_saveexec_b64 s[8:9], vcc
	s_cbranch_execz .LBB0_323
	s_bcnt1_i32_b64 s6, s[6:7]
	v_mov_b32_e32 v1, 0x2000
	v_mov_b32_e32 v2, s6
	global_atomic_add v1, v2, s[4:5] offset:1024

; #define PG8_STAGE(bufoff, gbase, voff) do { _Pragma("unroll") for (int _i = 0; _i < 2; ++_i) \
;         __builtin_amdgcn_global_load_lds((const unsigned*)((const char*)(gbase) + (voff)[_i]), (PG8_LAS unsigned*)(lds + (bufoff) + ldsw + _i * 8192), 16, 0, 0); } while (0)
; #define PG8_LDA(dst, b, h) do { _Pragma("unroll") for (int m = 0; m < 4; ++m) { const i32x4 _l = *(const PG8_LAS i32x4*)(lds + PG8_SA(b, h) + aoff + m * 2048), _h = *(const PG8_LAS i32x4*)(lds + PG8_SA(b, h) + aoff + m * 2048 + 512); dst[m] = PG8_CAT(_l, _h); } } while (0)
; #define PG8_LDB(dst, b, h) do { _Pragma("unroll") for (int n = 0; n < 2; ++n) { const i32x4 _l = *(const PG8_LAS i32x4*)(lds + PG8_SB(b, h) + boff + n * 2048), _h = *(const PG8_LAS i32x4*)(lds + PG8_SB(b, h) + boff + n * 2048 + 512); dst[n] = PG8_CAT(_l, _h); } } while (0)
; #define PG8_WAIT_V(n) asm volatile("s_waitcnt vmcnt(" #n ")" ::: "memory")
; #define PG8_WAIT_L(n) asm volatile("s_waitcnt lgkmcnt(" #n ")" ::: "memory")
; #define PG8_BAR __builtin_amdgcn_s_barrier()
; #define PG8_SCHED __builtin_amdgcn_sched_barrier(0)
;     ...
;         for (int t = 0; t < nt; t += 2) {
;             const bool last = (t == nt - 2);
;             const char* a1 = cA + (size_t)(t + 1) * kstep;
;             const char* a2 = last ? nA : cA + (size_t)(t + 2) * kstep; const char* b2 = last ? nB : cB + (size_t)(t + 2) * kstep;
;             const char* a3 = a2 + kstep; const char* b3 = b2 + kstep;
;             if (last && has_next) S.a_ready(nxt);
;             if constexpr (Epi::MIDK) { if (t == nt / 2) { if constexpr (ES == 1) asm volatile("s_nop 15\n\ts_nop 15" ::: "memory"); E.mid(acc, cur, wr, wc, fr, fq); } }
;             PG8_LDB(B0, 0, 0); PG8_LDB(B1, 0, 1); PG8_SCHED; PG8_LDA(At, 0, 0); PG8_STAGE(PG8_SA(1, 1), a1 + hstepA, voffA);
;             PG8_WAIT_V(8); PG8_WAIT_L(0); PG8_BAR; PG8_MMA(0, 0, At, B0); PG8_MMA(0, 1, At, B1); PG8_BAR; PG8_SCHED;
;             PG8_LDA(At, 0, 1); PG8_STAGE(PG8_SB(0, 0), b2, voffB); PG8_STAGE(PG8_SB(0, 1), b2 + hstepB, voffB); PG8_STAGE(PG8_SA(0, 0), a2, voffA);
;             PG8_WAIT_V(8); PG8_WAIT_L(0); PG8_BAR; PG8_MMA(1, 0, At, B0); PG8_MMA(1, 1, At, B1); PG8_BAR; PG8_SCHED;
.LBB0_460:
	ds_read_b128 v[166:169], v158
	ds_read_b128 v[170:173], v158 offset:512
	ds_read_b128 v[174:177], v158 offset:2048
	ds_read_b128 v[188:191], v158 offset:2560
	ds_read_b128 v[192:195], v159
	ds_read_b128 v[196:199], v159 offset:512
	ds_read_b128 v[200:203], v159 offset:2048
	ds_read_b128 v[204:207], v159 offset:2560
	s_add_u32 s40, s38, 0x100
	s_addc_u32 s41, s39, 0
	s_cmp_eq_u32 s53, 60
	s_cselect_b32 s47, s23, s41
	s_cselect_b32 s46, s35, s40
	s_cselect_b32 s43, s25, s52
	s_cselect_b32 s42, s50, s51
	s_add_i32 m0, s11, 0xc000
	ds_read_b128 v[208:211], v160
	ds_read_b128 v[212:215], v160 offset:512
	ds_read_b128 v[216:219], v160 offset:2048
	ds_read_b128 v[220:223], v160 offset:2560
	ds_read_b128 v[224:227], v160 offset:4096
	ds_read_b128 v[228:231], v160 offset:4608
	ds_read_b128 v[232:235], v160 offset:6144
	ds_read_b128 v[236:239], v160 offset:6656
	global_load_lds_dwordx4 v138, s[38:39]
	s_add_i32 m0, s11, 0xe000
	s_nop 0
	global_load_lds_dwordx4 v140, s[38:39]
	s_waitcnt vmcnt(8)
	s_waitcnt lgkmcnt(0)
	s_barrier
	s_setprio 1
	s_waitcnt lgkmcnt(0)
	v_mfma_f32_16x16x32_bf16 v[126:129], v[166:169], v[208:211], v[126:129]
	v_mfma_f32_16x16x32_bf16 v[122:125], v[174:177], v[208:211], v[122:125]
	v_mfma_f32_16x16x32_bf16 v[110:113], v[166:169], v[216:219], v[110:113]
	v_mfma_f32_16x16x32_bf16 v[106:109], v[174:177], v[216:219], v[106:109]
	v_mfma_f32_16x16x32_bf16 v[94:97], v[166:169], v[224:227], v[94:97]
	v_mfma_f32_16x16x32_bf16 v[90:93], v[174:177], v[224:227], v[90:93]
	v_mfma_f32_16x16x32_bf16 v[78:81], v[166:169], v[232:235], v[78:81]
	v_mfma_f32_16x16x32_bf16 v[74:77], v[174:177], v[232:235], v[74:77]
	v_mfma_f32_16x16x32_bf16 v[126:129], v[170:173], v[212:215], v[126:129]
	v_mfma_f32_16x16x32_bf16 v[122:125], v[188:191], v[212:215], v[122:125]
	v_mfma_f32_16x16x32_bf16 v[110:113], v[170:173], v[220:223], v[110:113]
	v_mfma_f32_16x16x32_bf16 v[106:109], v[188:191], v[220:223], v[106:109]
	v_mfma_f32_16x16x32_bf16 v[94:97], v[170:173], v[228:231], v[94:97]
	v_mfma_f32_16x16x32_bf16 v[90:93], v[188:191], v[228:231], v[90:93]
	v_mfma_f32_16x16x32_bf16 v[78:81], v[170:173], v[236:239], v[78:81]
	v_mfma_f32_16x16x32_bf16 v[74:77], v[188:191], v[236:239], v[74:77]
	s_setprio 0
	s_setprio 1
	v_mfma_f32_16x16x32_bf16 v[118:121], v[192:195], v[208:211], v[118:121]
	v_mfma_f32_16x16x32_bf16 v[114:117], v[200:203], v[208:211], v[114:117]
	v_mfma_f32_16x16x32_bf16 v[102:105], v[192:195], v[216:219], v[102:105]
	v_mfma_f32_16x16x32_bf16 v[98:101], v[200:203], v[216:219], v[98:101]
	v_mfma_f32_16x16x32_bf16 v[86:89], v[192:195], v[224:227], v[86:89]
	v_mfma_f32_16x16x32_bf16 v[82:85], v[200:203], v[224:227], v[82:85]
	v_mfma_f32_16x16x32_bf16 v[70:73], v[192:195], v[232:235], v[70:73]
	v_mfma_f32_16x16x32_bf16 v[66:69], v[200:203], v[232:235], v[66:69]
	v_mfma_f32_16x16x32_bf16 v[118:121], v[196:199], v[212:215], v[118:121]
	v_mfma_f32_16x16x32_bf16 v[114:117], v[204:207], v[212:215], v[114:117]
	v_mfma_f32_16x16x32_bf16 v[102:105], v[196:199], v[220:223], v[102:105]
	v_mfma_f32_16x16x32_bf16 v[98:101], v[204:207], v[220:223], v[98:101]
	v_mfma_f32_16x16x32_bf16 v[86:89], v[196:199], v[228:231], v[86:89]
	v_mfma_f32_16x16x32_bf16 v[82:85], v[204:207], v[228:231], v[82:85]
	v_mfma_f32_16x16x32_bf16 v[70:73], v[196:199], v[236:239], v[70:73]
	v_mfma_f32_16x16x32_bf16 v[66:69], v[204:207], v[236:239], v[66:69]
	s_setprio 0
	s_barrier
	s_add_i32 s38, s37, s9
	s_mov_b32 m0, s38
	ds_read_b128 v[208:211], v160 offset:16384
	ds_read_b128 v[212:215], v160 offset:16896
	ds_read_b128 v[216:219], v160 offset:18432
	ds_read_b128 v[220:223], v160 offset:18944
	ds_read_b128 v[224:227], v160 offset:20480
	ds_read_b128 v[228:231], v160 offset:20992
	ds_read_b128 v[232:235], v160 offset:22528
	ds_read_b128 v[236:239], v160 offset:23040
	global_load_lds_dwordx4 v132, s[42:43]
	s_add_i32 m0, s38, 0x2000
	s_add_u32 s38, s42, 0x100000
	v_lshl_add_u64 v[178:179], s[42:43], 0, v[136:137]
	s_addc_u32 s39, s43, 0
	s_add_i32 s54, s48, s9
	global_load_lds_dwordx4 v136, s[42:43]
	s_mov_b32 m0, s54
	v_lshl_add_u64 v[242:243], s[46:47], 0, v[134:135]
	global_load_lds_dwordx4 v132, s[38:39]
	s_add_i32 m0, s54, 0x2000
	s_nop 0
	global_load_lds_dwordx4 v136, s[38:39]
	s_mov_b32 m0, s11
	s_nop 0
	global_load_lds_dwordx4 v130, s[46:47]
	s_mov_b32 m0, s13
	s_nop 0
	global_load_lds_dwordx4 v134, s[46:47]
	s_waitcnt vmcnt(8)
	s_waitcnt lgkmcnt(0)
	s_barrier
	s_setprio 1
	s_waitcnt lgkmcnt(0)
	v_mfma_f32_16x16x32_bf16 v[62:65], v[166:169], v[208:211], v[62:65]
	v_mfma_f32_16x16x32_bf16 v[58:61], v[174:177], v[208:211], v[58:61]
	v_mfma_f32_16x16x32_bf16 v[46:49], v[166:169], v[216:219], v[46:49]
	v_mfma_f32_16x16x32_bf16 v[42:45], v[174:177], v[216:219], v[42:45]
	v_mfma_f32_16x16x32_bf16 v[30:33], v[166:169], v[224:227], v[30:33]
	v_mfma_f32_16x16x32_bf16 v[26:29], v[174:177], v[224:227], v[26:29]
	v_mfma_f32_16x16x32_bf16 v[14:17], v[166:169], v[232:235], v[14:17]
	v_mfma_f32_16x16x32_bf16 v[10:13], v[174:177], v[232:235], v[10:13]
	v_mfma_f32_16x16x32_bf16 v[62:65], v[170:173], v[212:215], v[62:65]
	v_mfma_f32_16x16x32_bf16 v[58:61], v[188:191], v[212:215], v[58:61]
	v_mfma_f32_16x16x32_bf16 v[46:49], v[170:173], v[220:223], v[46:49]
	v_mfma_f32_16x16x32_bf16 v[42:45], v[188:191], v[220:223], v[42:45]
	v_mfma_f32_16x16x32_bf16 v[30:33], v[170:173], v[228:231], v[30:33]
	v_mfma_f32_16x16x32_bf16 v[26:29], v[188:191], v[228:231], v[26:29]
	v_mfma_f32_16x16x32_bf16 v[14:17], v[170:173], v[236:239], v[14:17]
	v_mfma_f32_16x16x32_bf16 v[10:13], v[188:191], v[236:239], v[10:13]
	s_setprio 0
	s_setprio 1
	v_mfma_f32_16x16x32_bf16 v[54:57], v[192:195], v[208:211], v[54:57]
	v_mfma_f32_16x16x32_bf16 v[50:53], v[200:203], v[208:211], v[50:53]
	v_mfma_f32_16x16x32_bf16 v[38:41], v[192:195], v[216:219], v[38:41]
	v_mfma_f32_16x16x32_bf16 v[34:37], v[200:203], v[216:219], v[34:37]
	v_mfma_f32_16x16x32_bf16 v[22:25], v[192:195], v[224:227], v[22:25]
	v_mfma_f32_16x16x32_bf16 v[18:21], v[200:203], v[224:227], v[18:21]
	v_mfma_f32_16x16x32_bf16 v[6:9], v[192:195], v[232:235], v[6:9]
	v_mfma_f32_16x16x32_bf16 v[2:5], v[200:203], v[232:235], v[2:5]
	v_mfma_f32_16x16x32_bf16 v[54:57], v[196:199], v[212:215], v[54:57]
	v_mfma_f32_16x16x32_bf16 v[50:53], v[204:207], v[212:215], v[50:53]
	v_mfma_f32_16x16x32_bf16 v[38:41], v[196:199], v[220:223], v[38:41]
	v_mfma_f32_16x16x32_bf16 v[34:37], v[204:207], v[220:223], v[34:37]
	v_mfma_f32_16x16x32_bf16 v[22:25], v[196:199], v[228:231], v[22:25]
	v_mfma_f32_16x16x32_bf16 v[18:21], v[204:207], v[228:231], v[18:21]
	v_mfma_f32_16x16x32_bf16 v[6:9], v[196:199], v[236:239], v[6:9]
	v_mfma_f32_16x16x32_bf16 v[2:5], v[204:207], v[236:239], v[2:5]
	s_setprio 0
	s_barrier
; #define PG8_STAGE(bufoff, gbase, voff) do { _Pragma("unroll") for (int _i = 0; _i < 2; ++_i) \
;         __builtin_amdgcn_global_load_lds((const unsigned*)((const char*)(gbase) + (voff)[_i]), (PG8_LAS unsigned*)(lds + (bufoff) + ldsw + _i * 8192), 16, 0, 0); } while (0)
; #define PG8_LDA(dst, b, h) do { _Pragma("unroll") for (int m = 0; m < 4; ++m) { const i32x4 _l = *(const PG8_LAS i32x4*)(lds + PG8_SA(b, h) + aoff + m * 2048), _h = *(const PG8_LAS i32x4*)(lds + PG8_SA(b, h) + aoff + m * 2048 + 512); dst[m] = PG8_CAT(_l, _h); } } while (0)
; #define PG8_LDB(dst, b, h) do { _Pragma("unroll") for (int n = 0; n < 2; ++n) { const i32x4 _l = *(const PG8_LAS i32x4*)(lds + PG8_SB(b, h) + boff + n * 2048), _h = *(const PG8_LAS i32x4*)(lds + PG8_SB(b, h) + boff + n * 2048 + 512); dst[n] = PG8_CAT(_l, _h); } } while (0)
; #define PG8_WAIT_V(n) asm volatile("s_waitcnt vmcnt(" #n ")" ::: "memory")
; #define PG8_WAIT_L(n) asm volatile("s_waitcnt lgkmcnt(" #n ")" ::: "memory")
; #define PG8_BAR __builtin_amdgcn_s_barrier()
; #define PG8_SCHED __builtin_amdgcn_sched_barrier(0)
;     ...
;             PG8_LDB(B0, 1, 0); PG8_LDB(B1, 1, 1); PG8_SCHED; PG8_LDA(At, 1, 0); PG8_STAGE(PG8_SA(0, 1), a2 + hstepA, voffA);
;             PG8_WAIT_V(8); PG8_WAIT_L(0); PG8_BAR; PG8_MMA(0, 0, At, B0); PG8_MMA(0, 1, At, B1); PG8_BAR; PG8_SCHED;
;             PG8_LDA(At, 1, 1); PG8_STAGE(PG8_SB(1, 0), b3, voffB); PG8_STAGE(PG8_SB(1, 1), b3 + hstepB, voffB); PG8_STAGE(PG8_SA(1, 0), a3, voffA);
;             PG8_WAIT_V(8); PG8_WAIT_L(0); PG8_BAR; PG8_MMA(1, 0, At, B0); PG8_MMA(1, 1, At, B1); PG8_BAR; PG8_SCHED;
;         }
	s_add_i32 s54, 0, 0x18000
	v_add_u32_e32 v161, s54, v156
	s_add_i32 s55, 0, 0x1c000
	ds_read_b128 v[166:169], v161
	ds_read_b128 v[170:173], v161 offset:512
	ds_read_b128 v[174:177], v161 offset:2048
	ds_read_b128 v[188:191], v161 offset:2560
	v_add_u32_e32 v161, s55, v156
	ds_read_b128 v[192:195], v161
	ds_read_b128 v[196:199], v161 offset:512
	ds_read_b128 v[200:203], v161 offset:2048
	ds_read_b128 v[204:207], v161 offset:2560
	s_add_u32 s38, s46, 0x100000
	s_addc_u32 s39, s47, 0
	s_mov_b32 m0, s15
	ds_read_b128 v[208:211], v160 offset:32768
	ds_read_b128 v[212:215], v160 offset:33280
	ds_read_b128 v[216:219], v160 offset:34816
	ds_read_b128 v[220:223], v160 offset:35328
	ds_read_b128 v[224:227], v160 offset:36864
	ds_read_b128 v[228:231], v160 offset:37376
	ds_read_b128 v[232:235], v160 offset:38912
	ds_read_b128 v[236:239], v160 offset:39424
	global_load_lds_dwordx4 v130, s[38:39]
	s_mov_b32 m0, s17
	s_nop 0
	global_load_lds_dwordx4 v134, s[38:39]
	s_waitcnt vmcnt(8)
	s_waitcnt lgkmcnt(0)
	s_barrier
	s_setprio 1
	s_waitcnt lgkmcnt(0)
	v_mfma_f32_16x16x32_bf16 v[126:129], v[166:169], v[208:211], v[126:129]
	v_mfma_f32_16x16x32_bf16 v[122:125], v[174:177], v[208:211], v[122:125]
	v_mfma_f32_16x16x32_bf16 v[110:113], v[166:169], v[216:219], v[110:113]
	v_mfma_f32_16x16x32_bf16 v[106:109], v[174:177], v[216:219], v[106:109]
	v_mfma_f32_16x16x32_bf16 v[94:97], v[166:169], v[224:227], v[94:97]
	v_mfma_f32_16x16x32_bf16 v[90:93], v[174:177], v[224:227], v[90:93]
	v_mfma_f32_16x16x32_bf16 v[78:81], v[166:169], v[232:235], v[78:81]
	v_mfma_f32_16x16x32_bf16 v[74:77], v[174:177], v[232:235], v[74:77]
	v_mfma_f32_16x16x32_bf16 v[126:129], v[170:173], v[212:215], v[126:129]
	v_mfma_f32_16x16x32_bf16 v[122:125], v[188:191], v[212:215], v[122:125]
	v_mfma_f32_16x16x32_bf16 v[110:113], v[170:173], v[220:223], v[110:113]
	v_mfma_f32_16x16x32_bf16 v[106:109], v[188:191], v[220:223], v[106:109]
	v_mfma_f32_16x16x32_bf16 v[94:97], v[170:173], v[228:231], v[94:97]
	v_mfma_f32_16x16x32_bf16 v[90:93], v[188:191], v[228:231], v[90:93]
	v_mfma_f32_16x16x32_bf16 v[78:81], v[170:173], v[236:239], v[78:81]
	v_mfma_f32_16x16x32_bf16 v[74:77], v[188:191], v[236:239], v[74:77]
	s_setprio 0
	s_setprio 1
	v_mfma_f32_16x16x32_bf16 v[118:121], v[192:195], v[208:211], v[118:121]
	v_mfma_f32_16x16x32_bf16 v[114:117], v[200:203], v[208:211], v[114:117]
	v_mfma_f32_16x16x32_bf16 v[102:105], v[192:195], v[216:219], v[102:105]
	v_mfma_f32_16x16x32_bf16 v[98:101], v[200:203], v[216:219], v[98:101]
	v_mfma_f32_16x16x32_bf16 v[86:89], v[192:195], v[224:227], v[86:89]
	v_mfma_f32_16x16x32_bf16 v[82:85], v[200:203], v[224:227], v[82:85]
	v_mfma_f32_16x16x32_bf16 v[70:73], v[192:195], v[232:235], v[70:73]
	v_mfma_f32_16x16x32_bf16 v[66:69], v[200:203], v[232:235], v[66:69]
	v_mfma_f32_16x16x32_bf16 v[118:121], v[196:199], v[212:215], v[118:121]
	v_mfma_f32_16x16x32_bf16 v[114:117], v[204:207], v[212:215], v[114:117]
	v_mfma_f32_16x16x32_bf16 v[102:105], v[196:199], v[220:223], v[102:105]
	v_mfma_f32_16x16x32_bf16 v[98:101], v[204:207], v[220:223], v[98:101]
	v_mfma_f32_16x16x32_bf16 v[86:89], v[196:199], v[228:231], v[86:89]
	v_mfma_f32_16x16x32_bf16 v[82:85], v[204:207], v[228:231], v[82:85]
	v_mfma_f32_16x16x32_bf16 v[70:73], v[196:199], v[236:239], v[70:73]
	v_mfma_f32_16x16x32_bf16 v[66:69], v[204:207], v[236:239], v[66:69]
	s_setprio 0
	s_barrier
	s_add_i32 s38, s54, s9
	s_add_i32 m0, s38, 0xffffff80
	ds_read_b128 v[208:211], v160 offset:49152
	ds_read_b128 v[212:215], v160 offset:49664
	ds_read_b128 v[216:219], v160 offset:51200
	ds_read_b128 v[220:223], v160 offset:51712
	ds_read_b128 v[224:227], v160 offset:53248
	ds_read_b128 v[228:231], v160 offset:53760
	ds_read_b128 v[232:235], v160 offset:55296
	ds_read_b128 v[236:239], v160 offset:55808
	global_load_lds_dwordx4 v132, s[42:43] offset:128
	s_add_i32 m0, s38, 0x2000
	s_add_u32 s38, s42, 0x100080
	v_lshl_add_u64 v[162:163], v[178:179], 0, s[4:5]
	s_addc_u32 s39, s43, 0
	s_add_i32 s42, s55, s9
	global_load_lds_dwordx4 v[162:163], off
	s_mov_b32 m0, s42
	s_nop 0
	global_load_lds_dwordx4 v132, s[38:39]
	s_add_i32 m0, s42, 0x2000
	s_nop 0
	global_load_lds_dwordx4 v136, s[38:39]
	s_add_i32 m0, s21, 0xffffff80
	s_nop 0
	global_load_lds_dwordx4 v130, s[46:47] offset:128
	v_lshl_add_u64 v[162:163], v[242:243], 0, s[4:5]
	s_add_i32 m0, s33, 0xffffff80
	s_nop 0
	global_load_lds_dwordx4 v134, s[46:47] offset:128
	s_waitcnt vmcnt(8)
	s_waitcnt lgkmcnt(0)
	s_barrier
	s_setprio 1
	s_waitcnt lgkmcnt(0)
	v_mfma_f32_16x16x32_bf16 v[62:65], v[166:169], v[208:211], v[62:65]
	v_mfma_f32_16x16x32_bf16 v[58:61], v[174:177], v[208:211], v[58:61]
	v_mfma_f32_16x16x32_bf16 v[46:49], v[166:169], v[216:219], v[46:49]
	v_mfma_f32_16x16x32_bf16 v[42:45], v[174:177], v[216:219], v[42:45]
	v_mfma_f32_16x16x32_bf16 v[30:33], v[166:169], v[224:227], v[30:33]
	v_mfma_f32_16x16x32_bf16 v[26:29], v[174:177], v[224:227], v[26:29]
	v_mfma_f32_16x16x32_bf16 v[14:17], v[166:169], v[232:235], v[14:17]
	v_mfma_f32_16x16x32_bf16 v[10:13], v[174:177], v[232:235], v[10:13]
	v_mfma_f32_16x16x32_bf16 v[62:65], v[170:173], v[212:215], v[62:65]
	v_mfma_f32_16x16x32_bf16 v[58:61], v[188:191], v[212:215], v[58:61]
	v_mfma_f32_16x16x32_bf16 v[46:49], v[170:173], v[220:223], v[46:49]
	v_mfma_f32_16x16x32_bf16 v[42:45], v[188:191], v[220:223], v[42:45]
	v_mfma_f32_16x16x32_bf16 v[30:33], v[170:173], v[228:231], v[30:33]
	v_mfma_f32_16x16x32_bf16 v[26:29], v[188:191], v[228:231], v[26:29]
	v_mfma_f32_16x16x32_bf16 v[14:17], v[170:173], v[236:239], v[14:17]
	v_mfma_f32_16x16x32_bf16 v[10:13], v[188:191], v[236:239], v[10:13]
	s_setprio 0
	s_setprio 1
	v_mfma_f32_16x16x32_bf16 v[54:57], v[192:195], v[208:211], v[54:57]
	v_mfma_f32_16x16x32_bf16 v[50:53], v[200:203], v[208:211], v[50:53]
	v_mfma_f32_16x16x32_bf16 v[38:41], v[192:195], v[216:219], v[38:41]
	v_mfma_f32_16x16x32_bf16 v[34:37], v[200:203], v[216:219], v[34:37]
	v_mfma_f32_16x16x32_bf16 v[22:25], v[192:195], v[224:227], v[22:25]
	v_mfma_f32_16x16x32_bf16 v[18:21], v[200:203], v[224:227], v[18:21]
	v_mfma_f32_16x16x32_bf16 v[6:9], v[192:195], v[232:235], v[6:9]
	v_mfma_f32_16x16x32_bf16 v[2:5], v[200:203], v[232:235], v[2:5]
	v_mfma_f32_16x16x32_bf16 v[54:57], v[196:199], v[212:215], v[54:57]
	v_mfma_f32_16x16x32_bf16 v[50:53], v[204:207], v[212:215], v[50:53]
	v_mfma_f32_16x16x32_bf16 v[38:41], v[196:199], v[220:223], v[38:41]
	v_mfma_f32_16x16x32_bf16 v[34:37], v[204:207], v[220:223], v[34:37]
	v_mfma_f32_16x16x32_bf16 v[22:25], v[196:199], v[228:231], v[22:25]
	v_mfma_f32_16x16x32_bf16 v[18:21], v[204:207], v[228:231], v[18:21]
	v_mfma_f32_16x16x32_bf16 v[6:9], v[196:199], v[236:239], v[6:9]
	v_mfma_f32_16x16x32_bf16 v[2:5], v[204:207], v[236:239], v[2:5]
	s_setprio 0
	s_barrier
	s_add_i32 s53, s53, 2
	s_add_u32 s51, s51, 0x100
	s_addc_u32 s52, s52, 0
	s_cmp_gt_u32 s53, 61
	s_mov_b64 s[38:39], s[40:41]
	s_cbranch_scc0 .LBB0_460
	s_and_b64 vcc, exec, s[6:7]
	s_cbranch_vccz .LBB0_463
	s_barrier

; #define PG8_STAGE(bufoff, gbase, voff) do { _Pragma("unroll") for (int _i = 0; _i < 2; ++_i) \
;         __builtin_amdgcn_global_load_lds((const unsigned*)((const char*)(gbase) + (voff)[_i]), (PG8_LAS unsigned*)(lds + (bufoff) + ldsw + _i * 8192), 16, 0, 0); } while (0)
; #define PG8_LDA(dst, b, h) do { _Pragma("unroll") for (int m = 0; m < 4; ++m) { const i32x4 _l = *(const PG8_LAS i32x4*)(lds + PG8_SA(b, h) + aoff + m * 2048), _h = *(const PG8_LAS i32x4*)(lds + PG8_SA(b, h) + aoff + m * 2048 + 512); dst[m] = PG8_CAT(_l, _h); } } while (0)
; #define PG8_LDB(dst, b, h) do { _Pragma("unroll") for (int n = 0; n < 2; ++n) { const i32x4 _l = *(const PG8_LAS i32x4*)(lds + PG8_SB(b, h) + boff + n * 2048), _h = *(const PG8_LAS i32x4*)(lds + PG8_SB(b, h) + boff + n * 2048 + 512); dst[n] = PG8_CAT(_l, _h); } } while (0)
; #define PG8_WAIT_V(n) asm volatile("s_waitcnt vmcnt(" #n ")" ::: "memory")
; #define PG8_WAIT_L(n) asm volatile("s_waitcnt lgkmcnt(" #n ")" ::: "memory")
; #define PG8_BAR __builtin_amdgcn_s_barrier()
; #define PG8_SCHED __builtin_amdgcn_sched_barrier(0)
;     ...
;         for (int t = 0; t < nt; t += 2) {
;             const bool last = (t == nt - 2);
;             const char* a1 = cA + (size_t)(t + 1) * kstep;
;             const char* a2 = last ? nA : cA + (size_t)(t + 2) * kstep; const char* b2 = last ? nB : cB + (size_t)(t + 2) * kstep;
;             const char* a3 = a2 + kstep; const char* b3 = b2 + kstep;
;             if (last && has_next) S.a_ready(nxt);
;             if constexpr (Epi::MIDK) { if (t == nt / 2) { if constexpr (ES == 1) asm volatile("s_nop 15\n\ts_nop 15" ::: "memory"); E.mid(acc, cur, wr, wc, fr, fq); } }
;             PG8_LDB(B0, 0, 0); PG8_LDB(B1, 0, 1); PG8_SCHED; PG8_LDA(At, 0, 0); PG8_STAGE(PG8_SA(1, 1), a1 + hstepA, voffA);
;             PG8_WAIT_V(8); PG8_WAIT_L(0); PG8_BAR; PG8_MMA(0, 0, At, B0); PG8_MMA(0, 1, At, B1); PG8_BAR; PG8_SCHED;
;             PG8_LDA(At, 0, 1); PG8_STAGE(PG8_SB(0, 0), b2, voffB); PG8_STAGE(PG8_SB(0, 1), b2 + hstepB, voffB); PG8_STAGE(PG8_SA(0, 0), a2, voffA);
;             PG8_WAIT_V(8); PG8_WAIT_L(0); PG8_BAR; PG8_MMA(1, 0, At, B0); PG8_MMA(1, 1, At, B1); PG8_BAR; PG8_SCHED;
.LBB0_593:
	s_add_u32 s76, s74, 0x100
	s_addc_u32 s77, s75, 0
	s_add_i32 vcc_hi, 0, 0x10000
	s_cmp_eq_u32 vcc_lo, 28
	s_cselect_b32 s81, s61, s77
	s_cselect_b32 s80, s71, s76
	s_cselect_b32 s79, s63, s97
	s_cselect_b32 s78, s95, s96
	s_add_i32 s51, 0, 0x14000
	v_add_u32_e32 v4, vcc_hi, v203
	v_add_u32_e32 v16, s51, v203
	ds_read_b128 v[20:23], v4
	ds_read_b128 v[24:27], v4 offset:512
	ds_read_b128 v[28:31], v4 offset:2048
	ds_read_b128 v[32:35], v4 offset:2560
	ds_read_b128 v[4:7], v16
	ds_read_b128 v[8:11], v16 offset:512
	ds_read_b128 v[12:15], v16 offset:2048
	ds_read_b128 v[16:19], v16 offset:2560
	s_add_i32 m0, s73, 0xc000
	ds_read_b128 v[206:209], v205
	ds_read_b128 v[210:213], v205 offset:512
	ds_read_b128 v[214:217], v205 offset:2048
	ds_read_b128 v[218:221], v205 offset:2560
	ds_read_b128 v[222:225], v205 offset:4096
	ds_read_b128 v[226:229], v205 offset:4608
	ds_read_b128 v[230:233], v205 offset:6144
	ds_read_b128 v[234:237], v205 offset:6656
	global_load_lds_dwordx4 v174, s[74:75]
	s_add_i32 m0, s73, 0xe000
	s_nop 0
	global_load_lds_dwordx4 v176, s[74:75]
	s_waitcnt vmcnt(8)
	s_waitcnt lgkmcnt(0)
	s_barrier
	s_setprio 1
	s_waitcnt lgkmcnt(0)
	v_mfma_f32_16x16x128_f8f6f4 v[160:163], v[20:27], v[206:213], v[160:163]
	v_mfma_f32_16x16x128_f8f6f4 v[156:159], v[28:35], v[206:213], v[156:159]
	v_mfma_f32_16x16x128_f8f6f4 v[144:147], v[20:27], v[214:221], v[144:147]
	v_mfma_f32_16x16x128_f8f6f4 v[140:143], v[28:35], v[214:221], v[140:143]
	v_mfma_f32_16x16x128_f8f6f4 v[128:131], v[20:27], v[222:229], v[128:131]
	v_mfma_f32_16x16x128_f8f6f4 v[124:127], v[28:35], v[222:229], v[124:127]
	v_mfma_f32_16x16x128_f8f6f4 v[112:115], v[20:27], v[230:237], v[112:115]
	v_mfma_f32_16x16x128_f8f6f4 v[108:111], v[28:35], v[230:237], v[108:111]
	s_setprio 0
	s_setprio 1
	v_mfma_f32_16x16x128_f8f6f4 v[152:155], v[4:11], v[206:213], v[152:155]
	v_mfma_f32_16x16x128_f8f6f4 v[148:151], v[12:19], v[206:213], v[148:151]
	v_mfma_f32_16x16x128_f8f6f4 v[136:139], v[4:11], v[214:221], v[136:139]
	v_mfma_f32_16x16x128_f8f6f4 v[132:135], v[12:19], v[214:221], v[132:135]
	v_mfma_f32_16x16x128_f8f6f4 v[120:123], v[4:11], v[222:229], v[120:123]
	v_mfma_f32_16x16x128_f8f6f4 v[116:119], v[12:19], v[222:229], v[116:119]
	v_mfma_f32_16x16x128_f8f6f4 v[104:107], v[4:11], v[230:237], v[104:107]
	v_mfma_f32_16x16x128_f8f6f4 v[100:103], v[12:19], v[230:237], v[100:103]
	s_setprio 0
	s_barrier
	s_add_i32 s74, vcc_hi, s88
	s_mov_b32 m0, s74
	ds_read_b128 v[206:209], v205 offset:16384
	ds_read_b128 v[210:213], v205 offset:16896
	ds_read_b128 v[214:217], v205 offset:18432
	ds_read_b128 v[218:221], v205 offset:18944
	ds_read_b128 v[222:225], v205 offset:20480
	ds_read_b128 v[226:229], v205 offset:20992
	ds_read_b128 v[230:233], v205 offset:22528
	ds_read_b128 v[234:237], v205 offset:23040
	global_load_lds_dwordx4 v168, s[78:79]
	s_add_i32 m0, s74, 0x2000
	s_add_u32 s74, s78, 0x80000
	s_addc_u32 s75, s79, 0
	s_add_i32 s51, s51, s88
	global_load_lds_dwordx4 v172, s[78:79]
	s_mov_b32 m0, s51
	s_nop 0
	global_load_lds_dwordx4 v168, s[74:75]
	s_add_i32 m0, s51, 0x2000
	s_nop 0
	global_load_lds_dwordx4 v172, s[74:75]
	s_mov_b32 m0, s73
	s_nop 0
	global_load_lds_dwordx4 v166, s[80:81]
	s_mov_b32 m0, s89
	s_nop 0
	global_load_lds_dwordx4 v170, s[80:81]
	s_waitcnt vmcnt(8)
	s_waitcnt lgkmcnt(0)
	s_barrier
	s_setprio 1
	s_waitcnt lgkmcnt(0)
	v_mfma_f32_16x16x128_f8f6f4 v[96:99], v[20:27], v[206:213], v[96:99]
	v_mfma_f32_16x16x128_f8f6f4 v[92:95], v[28:35], v[206:213], v[92:95]
	v_mfma_f32_16x16x128_f8f6f4 v[80:83], v[20:27], v[214:221], v[80:83]
	v_mfma_f32_16x16x128_f8f6f4 v[76:79], v[28:35], v[214:221], v[76:79]
	v_mfma_f32_16x16x128_f8f6f4 v[64:67], v[20:27], v[222:229], v[64:67]
	v_mfma_f32_16x16x128_f8f6f4 v[60:63], v[28:35], v[222:229], v[60:63]
	v_mfma_f32_16x16x128_f8f6f4 v[48:51], v[20:27], v[230:237], v[48:51]
	v_mfma_f32_16x16x128_f8f6f4 v[44:47], v[28:35], v[230:237], v[44:47]
	s_setprio 0
	s_setprio 1
	v_mfma_f32_16x16x128_f8f6f4 v[88:91], v[4:11], v[206:213], v[88:91]
	v_mfma_f32_16x16x128_f8f6f4 v[84:87], v[12:19], v[206:213], v[84:87]
	v_mfma_f32_16x16x128_f8f6f4 v[72:75], v[4:11], v[214:221], v[72:75]
	v_mfma_f32_16x16x128_f8f6f4 v[68:71], v[12:19], v[214:221], v[68:71]
	v_mfma_f32_16x16x128_f8f6f4 v[56:59], v[4:11], v[222:229], v[56:59]
	v_mfma_f32_16x16x128_f8f6f4 v[52:55], v[12:19], v[222:229], v[52:55]
	v_mfma_f32_16x16x128_f8f6f4 v[40:43], v[4:11], v[230:237], v[40:43]
	v_mfma_f32_16x16x128_f8f6f4 v[36:39], v[12:19], v[230:237], v[36:39]
	s_setprio 0
	s_barrier
; #define PG8_STAGE(bufoff, gbase, voff) do { _Pragma("unroll") for (int _i = 0; _i < 2; ++_i) \
;         __builtin_amdgcn_global_load_lds((const unsigned*)((const char*)(gbase) + (voff)[_i]), (PG8_LAS unsigned*)(lds + (bufoff) + ldsw + _i * 8192), 16, 0, 0); } while (0)
; #define PG8_LDA(dst, b, h) do { _Pragma("unroll") for (int m = 0; m < 4; ++m) { const i32x4 _l = *(const PG8_LAS i32x4*)(lds + PG8_SA(b, h) + aoff + m * 2048), _h = *(const PG8_LAS i32x4*)(lds + PG8_SA(b, h) + aoff + m * 2048 + 512); dst[m] = PG8_CAT(_l, _h); } } while (0)
; #define PG8_LDB(dst, b, h) do { _Pragma("unroll") for (int n = 0; n < 2; ++n) { const i32x4 _l = *(const PG8_LAS i32x4*)(lds + PG8_SB(b, h) + boff + n * 2048), _h = *(const PG8_LAS i32x4*)(lds + PG8_SB(b, h) + boff + n * 2048 + 512); dst[n] = PG8_CAT(_l, _h); } } while (0)
; #define PG8_WAIT_V(n) asm volatile("s_waitcnt vmcnt(" #n ")" ::: "memory")
; #define PG8_WAIT_L(n) asm volatile("s_waitcnt lgkmcnt(" #n ")" ::: "memory")
; #define PG8_BAR __builtin_amdgcn_s_barrier()
; #define PG8_SCHED __builtin_amdgcn_sched_barrier(0)
;     ...
;             PG8_LDB(B0, 1, 0); PG8_LDB(B1, 1, 1); PG8_SCHED; PG8_LDA(At, 1, 0); PG8_STAGE(PG8_SA(0, 1), a2 + hstepA, voffA);
;             PG8_WAIT_V(8); PG8_WAIT_L(0); PG8_BAR; PG8_MMA(0, 0, At, B0); PG8_MMA(0, 1, At, B1); PG8_BAR; PG8_SCHED;
;             PG8_LDA(At, 1, 1); PG8_STAGE(PG8_SB(1, 0), b3, voffB); PG8_STAGE(PG8_SB(1, 1), b3 + hstepB, voffB); PG8_STAGE(PG8_SA(1, 0), a3, voffA);
;             PG8_WAIT_V(8); PG8_WAIT_L(0); PG8_BAR; PG8_MMA(1, 0, At, B0); PG8_MMA(1, 1, At, B1); PG8_BAR; PG8_SCHED;
;         }
	s_add_i32 s51, 0, 0x18000
	s_add_i32 vcc_hi, 0, 0x1c000
	v_add_u32_e32 v16, s51, v203
	v_add_u32_e32 v32, vcc_hi, v203
	ds_read_b128 v[4:7], v16
	ds_read_b128 v[8:11], v16 offset:512
	ds_read_b128 v[12:15], v16 offset:2048
	ds_read_b128 v[16:19], v16 offset:2560
	ds_read_b128 v[20:23], v32
	ds_read_b128 v[24:27], v32 offset:512
	ds_read_b128 v[28:31], v32 offset:2048
	ds_read_b128 v[32:35], v32 offset:2560
	s_add_u32 s74, s80, 0x80000
	s_addc_u32 s75, s81, 0
	s_mov_b32 m0, s90
	ds_read_b128 v[206:209], v205 offset:32768
	ds_read_b128 v[210:213], v205 offset:33280
	ds_read_b128 v[214:217], v205 offset:34816
	ds_read_b128 v[218:221], v205 offset:35328
	ds_read_b128 v[222:225], v205 offset:36864
	ds_read_b128 v[226:229], v205 offset:37376
	ds_read_b128 v[230:233], v205 offset:38912
	ds_read_b128 v[234:237], v205 offset:39424
	global_load_lds_dwordx4 v166, s[74:75]
	s_mov_b32 m0, s91
	s_nop 0
	global_load_lds_dwordx4 v170, s[74:75]
	s_waitcnt vmcnt(8)
	s_waitcnt lgkmcnt(0)
	s_barrier
	s_setprio 1
	s_waitcnt lgkmcnt(0)
	v_mfma_f32_16x16x128_f8f6f4 v[160:163], v[4:11], v[206:213], v[160:163]
	v_mfma_f32_16x16x128_f8f6f4 v[156:159], v[12:19], v[206:213], v[156:159]
	v_mfma_f32_16x16x128_f8f6f4 v[144:147], v[4:11], v[214:221], v[144:147]
	v_mfma_f32_16x16x128_f8f6f4 v[140:143], v[12:19], v[214:221], v[140:143]
	v_mfma_f32_16x16x128_f8f6f4 v[128:131], v[4:11], v[222:229], v[128:131]
	v_mfma_f32_16x16x128_f8f6f4 v[124:127], v[12:19], v[222:229], v[124:127]
	v_mfma_f32_16x16x128_f8f6f4 v[112:115], v[4:11], v[230:237], v[112:115]
	v_mfma_f32_16x16x128_f8f6f4 v[108:111], v[12:19], v[230:237], v[108:111]
	s_setprio 0
	s_setprio 1
	v_mfma_f32_16x16x128_f8f6f4 v[152:155], v[20:27], v[206:213], v[152:155]
	v_mfma_f32_16x16x128_f8f6f4 v[148:151], v[28:35], v[206:213], v[148:151]
	v_mfma_f32_16x16x128_f8f6f4 v[136:139], v[20:27], v[214:221], v[136:139]
	v_mfma_f32_16x16x128_f8f6f4 v[132:135], v[28:35], v[214:221], v[132:135]
	v_mfma_f32_16x16x128_f8f6f4 v[120:123], v[20:27], v[222:229], v[120:123]
	v_mfma_f32_16x16x128_f8f6f4 v[116:119], v[28:35], v[222:229], v[116:119]
	v_mfma_f32_16x16x128_f8f6f4 v[104:107], v[20:27], v[230:237], v[104:107]
	v_mfma_f32_16x16x128_f8f6f4 v[100:103], v[28:35], v[230:237], v[100:103]
	s_setprio 0
	s_barrier
	s_add_i32 s51, s51, s88
	s_add_i32 m0, s51, 0xffffff80
	ds_read_b128 v[206:209], v205 offset:49152
	ds_read_b128 v[210:213], v205 offset:49664
	ds_read_b128 v[214:217], v205 offset:51200
	ds_read_b128 v[218:221], v205 offset:51712
	ds_read_b128 v[222:225], v205 offset:53248
	ds_read_b128 v[226:229], v205 offset:53760
	ds_read_b128 v[230:233], v205 offset:55296
	ds_read_b128 v[234:237], v205 offset:55808
	global_load_lds_dwordx4 v168, s[78:79] offset:128
	s_add_i32 m0, s51, 0x1f80
	s_add_u32 s74, s78, 0x80080
	s_addc_u32 s75, s79, 0
	s_add_i32 s51, vcc_hi, s88
	global_load_lds_dwordx4 v172, s[78:79] offset:128
	s_mov_b32 m0, s51
	s_nop 0
	global_load_lds_dwordx4 v168, s[74:75]
	s_add_i32 m0, s51, 0x2000
	s_nop 0
	global_load_lds_dwordx4 v172, s[74:75]
	s_add_i32 m0, s92, 0xffffff80
	s_nop 0
	global_load_lds_dwordx4 v166, s[80:81] offset:128
	s_add_i32 m0, s93, 0xffffff80
	s_nop 0
	global_load_lds_dwordx4 v170, s[80:81] offset:128
	s_waitcnt vmcnt(8)
	s_waitcnt lgkmcnt(0)
	s_barrier
	s_setprio 1
	s_waitcnt lgkmcnt(0)
	v_mfma_f32_16x16x128_f8f6f4 v[96:99], v[4:11], v[206:213], v[96:99]
	v_mfma_f32_16x16x128_f8f6f4 v[92:95], v[12:19], v[206:213], v[92:95]
	v_mfma_f32_16x16x128_f8f6f4 v[80:83], v[4:11], v[214:221], v[80:83]
	v_mfma_f32_16x16x128_f8f6f4 v[76:79], v[12:19], v[214:221], v[76:79]
	v_mfma_f32_16x16x128_f8f6f4 v[64:67], v[4:11], v[222:229], v[64:67]
	v_mfma_f32_16x16x128_f8f6f4 v[60:63], v[12:19], v[222:229], v[60:63]
	v_mfma_f32_16x16x128_f8f6f4 v[48:51], v[4:11], v[230:237], v[48:51]
	v_mfma_f32_16x16x128_f8f6f4 v[44:47], v[12:19], v[230:237], v[44:47]
	s_setprio 0
	s_setprio 1
	v_mfma_f32_16x16x128_f8f6f4 v[88:91], v[20:27], v[206:213], v[88:91]
	v_mfma_f32_16x16x128_f8f6f4 v[84:87], v[28:35], v[206:213], v[84:87]
	v_mfma_f32_16x16x128_f8f6f4 v[72:75], v[20:27], v[214:221], v[72:75]
	v_mfma_f32_16x16x128_f8f6f4 v[68:71], v[28:35], v[214:221], v[68:71]
	v_mfma_f32_16x16x128_f8f6f4 v[56:59], v[20:27], v[222:229], v[56:59]
	v_mfma_f32_16x16x128_f8f6f4 v[52:55], v[28:35], v[222:229], v[52:55]
	v_mfma_f32_16x16x128_f8f6f4 v[40:43], v[20:27], v[230:237], v[40:43]
	v_mfma_f32_16x16x128_f8f6f4 v[36:39], v[28:35], v[230:237], v[36:39]
	s_setprio 0
	s_barrier
	s_add_i32 vcc_lo, vcc_lo, 2
	s_add_u32 s96, s96, 0x100
	s_addc_u32 s97, s97, 0
	s_cmp_gt_u32 vcc_lo, 29
	s_mov_b64 s[74:75], s[76:77]
	s_cbranch_scc0 .LBB0_593
	s_and_b64 vcc, exec, s[58:59]
	s_cbranch_vccz .LBB0_596
	s_barrier

; #define PG8_STAGE(bufoff, gbase, voff) do { _Pragma("unroll") for (int _i = 0; _i < 2; ++_i) \
;         __builtin_amdgcn_global_load_lds((const unsigned*)((const char*)(gbase) + (voff)[_i]), (PG8_LAS unsigned*)(lds + (bufoff) + ldsw + _i * 8192), 16, 0, 0); } while (0)
; #define PG8_LDA(dst, b, h) do { _Pragma("unroll") for (int m = 0; m < 4; ++m) { const i32x4 _l = *(const PG8_LAS i32x4*)(lds + PG8_SA(b, h) + aoff + m * 2048), _h = *(const PG8_LAS i32x4*)(lds + PG8_SA(b, h) + aoff + m * 2048 + 512); dst[m] = PG8_CAT(_l, _h); } } while (0)
; #define PG8_LDB(dst, b, h) do { _Pragma("unroll") for (int n = 0; n < 2; ++n) { const i32x4 _l = *(const PG8_LAS i32x4*)(lds + PG8_SB(b, h) + boff + n * 2048), _h = *(const PG8_LAS i32x4*)(lds + PG8_SB(b, h) + boff + n * 2048 + 512); dst[n] = PG8_CAT(_l, _h); } } while (0)
; #define PG8_WAIT_V(n) asm volatile("s_waitcnt vmcnt(" #n ")" ::: "memory")
; #define PG8_WAIT_L(n) asm volatile("s_waitcnt lgkmcnt(" #n ")" ::: "memory")
; #define PG8_BAR __builtin_amdgcn_s_barrier()
; #define PG8_SCHED __builtin_amdgcn_sched_barrier(0)
;     ...
;         for (int t = 0; t < nt; t += 2) {
;             const bool last = (t == nt - 2);
;             const char* a1 = cA + (size_t)(t + 1) * kstep;
;             const char* a2 = last ? nA : cA + (size_t)(t + 2) * kstep; const char* b2 = last ? nB : cB + (size_t)(t + 2) * kstep;
;             const char* a3 = a2 + kstep; const char* b3 = b2 + kstep;
;             if (last && has_next) S.a_ready(nxt);
;             if constexpr (Epi::MIDK) { if (t == nt / 2) { if constexpr (ES == 1) asm volatile("s_nop 15\n\ts_nop 15" ::: "memory"); E.mid(acc, cur, wr, wc, fr, fq); } }
;             PG8_LDB(B0, 0, 0); PG8_LDB(B1, 0, 1); PG8_SCHED; PG8_LDA(At, 0, 0); PG8_STAGE(PG8_SA(1, 1), a1 + hstepA, voffA);
;             PG8_WAIT_V(8); PG8_WAIT_L(0); PG8_BAR; PG8_MMA(0, 0, At, B0); PG8_MMA(0, 1, At, B1); PG8_BAR; PG8_SCHED;
;             PG8_LDA(At, 0, 1); PG8_STAGE(PG8_SB(0, 0), b2, voffB); PG8_STAGE(PG8_SB(0, 1), b2 + hstepB, voffB); PG8_STAGE(PG8_SA(0, 0), a2, voffA);
;             PG8_WAIT_V(8); PG8_WAIT_L(0); PG8_BAR; PG8_MMA(1, 0, At, B0); PG8_MMA(1, 1, At, B1); PG8_BAR; PG8_SCHED;
.LBB0_1708:
	v_add_u32_e32 v14, s49, v181
	v_add_u32_e32 v27, s50, v181
	s_add_u32 s34, s28, s30
	ds_read_b128 v[2:5], v14
	ds_read_b128 v[6:9], v14 offset:512
	ds_read_b128 v[10:13], v14 offset:2048
	ds_read_b128 v[14:17], v14 offset:2560
	ds_read_b128 v[18:21], v27
	ds_read_b128 v[22:25], v27 offset:512
	ds_read_b128 v[164:167], v27 offset:2048
	ds_read_b128 v[168:171], v27 offset:2560
	s_addc_u32 s35, s29, s31
	s_add_u32 s34, s34, 0x100
	s_addc_u32 s35, s35, 0
	s_add_u32 s58, s54, s30
	s_addc_u32 s59, s55, s31
	s_cmpk_eq_i32 s30, 0xf00
	s_cselect_b32 s37, s23, s35
	s_cselect_b32 s36, s52, s34
	s_cselect_b32 s35, s21, s59
	s_cselect_b32 s34, s53, s58
	v_lshl_add_u64 v[28:29], v[206:207], 0, s[30:31]
	s_add_i32 m0, s39, 0xc000
	ds_read_b128 v[210:213], v185
	ds_read_b128 v[214:217], v185 offset:512
	ds_read_b128 v[218:221], v185 offset:2048
	ds_read_b128 v[222:225], v185 offset:2560
	ds_read_b128 v[226:229], v185 offset:4096
	ds_read_b128 v[230:233], v185 offset:4608
	ds_read_b128 v[234:237], v185 offset:6144
	ds_read_b128 v[238:241], v185 offset:6656
	global_load_lds_dwordx4 v[28:29], off
	v_lshl_add_u64 v[28:29], v[208:209], 0, s[30:31]
	s_add_i32 m0, s39, 0xe000
	s_nop 0
	global_load_lds_dwordx4 v[28:29], off
	s_waitcnt vmcnt(8)
	s_waitcnt lgkmcnt(0)
	s_barrier
	s_setprio 1
	s_waitcnt lgkmcnt(0)
	v_mfma_f32_16x16x128_f8f6f4 v[154:157], v[2:9], v[210:217], v[154:157]
	v_mfma_f32_16x16x128_f8f6f4 v[150:153], v[10:17], v[210:217], v[150:153]
	v_mfma_f32_16x16x128_f8f6f4 v[138:141], v[2:9], v[218:225], v[138:141]
	v_mfma_f32_16x16x128_f8f6f4 v[134:137], v[10:17], v[218:225], v[134:137]
	v_mfma_f32_16x16x128_f8f6f4 v[122:125], v[2:9], v[226:233], v[122:125]
	v_mfma_f32_16x16x128_f8f6f4 v[118:121], v[10:17], v[226:233], v[118:121]
	v_mfma_f32_16x16x128_f8f6f4 v[106:109], v[2:9], v[234:241], v[106:109]
	v_mfma_f32_16x16x128_f8f6f4 v[102:105], v[10:17], v[234:241], v[102:105]
	s_setprio 0
	s_setprio 1
	v_mfma_f32_16x16x128_f8f6f4 v[146:149], v[18:25], v[210:217], v[146:149]
	v_mfma_f32_16x16x128_f8f6f4 v[142:145], v[164:171], v[210:217], v[142:145]
	v_mfma_f32_16x16x128_f8f6f4 v[130:133], v[18:25], v[218:225], v[130:133]
	v_mfma_f32_16x16x128_f8f6f4 v[126:129], v[164:171], v[218:225], v[126:129]
	v_mfma_f32_16x16x128_f8f6f4 v[114:117], v[18:25], v[226:233], v[114:117]
	v_mfma_f32_16x16x128_f8f6f4 v[110:113], v[164:171], v[226:233], v[110:113]
	v_mfma_f32_16x16x128_f8f6f4 v[98:101], v[18:25], v[234:241], v[98:101]
	v_mfma_f32_16x16x128_f8f6f4 v[94:97], v[164:171], v[234:241], v[94:97]
	s_setprio 0
	s_barrier
	s_add_i32 s58, s49, s38
	s_mov_b32 m0, s58
	ds_read_b128 v[210:213], v185 offset:16384
	ds_read_b128 v[214:217], v185 offset:16896
	ds_read_b128 v[218:221], v185 offset:18432
	ds_read_b128 v[222:225], v185 offset:18944
	ds_read_b128 v[226:229], v185 offset:20480
	ds_read_b128 v[230:233], v185 offset:20992
	ds_read_b128 v[234:237], v185 offset:22528
	ds_read_b128 v[238:241], v185 offset:23040
	global_load_lds_dwordx4 v176, s[34:35]
	s_add_i32 m0, s58, 0x2000
	s_add_u32 s58, s34, 0x80000
	v_lshl_add_u64 v[158:159], s[34:35], 0, v[188:189]
	s_addc_u32 s59, s35, 0
	s_add_i32 s60, s50, s38
	global_load_lds_dwordx4 v188, s[34:35]
	s_mov_b32 m0, s60
	v_lshl_add_u64 v[162:163], s[36:37], 0, v[178:179]
	global_load_lds_dwordx4 v176, s[58:59]
	s_add_i32 m0, s60, 0x2000
	s_nop 0
	global_load_lds_dwordx4 v188, s[58:59]
	v_lshl_add_u64 v[160:161], s[36:37], 0, v[174:175]
	s_mov_b32 m0, s39
	s_nop 0
	global_load_lds_dwordx4 v174, s[36:37]
	s_mov_b32 m0, s40
	s_nop 0
	global_load_lds_dwordx4 v178, s[36:37]
	s_waitcnt vmcnt(8)
	s_waitcnt lgkmcnt(0)
	s_barrier
	s_setprio 1
	s_waitcnt lgkmcnt(0)
	v_mfma_f32_16x16x128_f8f6f4 v[90:93], v[2:9], v[210:217], v[90:93]
	v_mfma_f32_16x16x128_f8f6f4 v[86:89], v[10:17], v[210:217], v[86:89]
	v_mfma_f32_16x16x128_f8f6f4 v[74:77], v[2:9], v[218:225], v[74:77]
	v_mfma_f32_16x16x128_f8f6f4 v[70:73], v[10:17], v[218:225], v[70:73]
	v_mfma_f32_16x16x128_f8f6f4 v[58:61], v[2:9], v[226:233], v[58:61]
	v_mfma_f32_16x16x128_f8f6f4 v[54:57], v[10:17], v[226:233], v[54:57]
	v_mfma_f32_16x16x128_f8f6f4 v[42:45], v[2:9], v[234:241], v[42:45]
	v_mfma_f32_16x16x128_f8f6f4 v[38:41], v[10:17], v[234:241], v[38:41]
	s_setprio 0
	s_setprio 1
	v_mfma_f32_16x16x128_f8f6f4 v[82:85], v[18:25], v[210:217], v[82:85]
	v_mfma_f32_16x16x128_f8f6f4 v[78:81], v[164:171], v[210:217], v[78:81]
	v_mfma_f32_16x16x128_f8f6f4 v[66:69], v[18:25], v[218:225], v[66:69]
	v_mfma_f32_16x16x128_f8f6f4 v[62:65], v[164:171], v[218:225], v[62:65]
	v_mfma_f32_16x16x128_f8f6f4 v[50:53], v[18:25], v[226:233], v[50:53]
	v_mfma_f32_16x16x128_f8f6f4 v[46:49], v[164:171], v[226:233], v[46:49]
	v_mfma_f32_16x16x128_f8f6f4 v[34:37], v[18:25], v[234:241], v[34:37]
	v_mfma_f32_16x16x128_f8f6f4 v[30:33], v[164:171], v[234:241], v[30:33]
	s_setprio 0
	s_barrier
; #define PG8_STAGE(bufoff, gbase, voff) do { _Pragma("unroll") for (int _i = 0; _i < 2; ++_i) \
;         __builtin_amdgcn_global_load_lds((const unsigned*)((const char*)(gbase) + (voff)[_i]), (PG8_LAS unsigned*)(lds + (bufoff) + ldsw + _i * 8192), 16, 0, 0); } while (0)
; #define PG8_LDA(dst, b, h) do { _Pragma("unroll") for (int m = 0; m < 4; ++m) { const i32x4 _l = *(const PG8_LAS i32x4*)(lds + PG8_SA(b, h) + aoff + m * 2048), _h = *(const PG8_LAS i32x4*)(lds + PG8_SA(b, h) + aoff + m * 2048 + 512); dst[m] = PG8_CAT(_l, _h); } } while (0)
; #define PG8_LDB(dst, b, h) do { _Pragma("unroll") for (int n = 0; n < 2; ++n) { const i32x4 _l = *(const PG8_LAS i32x4*)(lds + PG8_SB(b, h) + boff + n * 2048), _h = *(const PG8_LAS i32x4*)(lds + PG8_SB(b, h) + boff + n * 2048 + 512); dst[n] = PG8_CAT(_l, _h); } } while (0)
; #define PG8_WAIT_V(n) asm volatile("s_waitcnt vmcnt(" #n ")" ::: "memory")
; #define PG8_WAIT_L(n) asm volatile("s_waitcnt lgkmcnt(" #n ")" ::: "memory")
; #define PG8_BAR __builtin_amdgcn_s_barrier()
; #define PG8_SCHED __builtin_amdgcn_sched_barrier(0)
;     ...
;             PG8_LDB(B0, 1, 0); PG8_LDB(B1, 1, 1); PG8_SCHED; PG8_LDA(At, 1, 0); PG8_STAGE(PG8_SA(0, 1), a2 + hstepA, voffA);
;             PG8_WAIT_V(8); PG8_WAIT_L(0); PG8_BAR; PG8_MMA(0, 0, At, B0); PG8_MMA(0, 1, At, B1); PG8_BAR; PG8_SCHED;
;             PG8_LDA(At, 1, 1); PG8_STAGE(PG8_SB(1, 0), b3, voffB); PG8_STAGE(PG8_SB(1, 1), b3 + hstepB, voffB); PG8_STAGE(PG8_SA(1, 0), a3, voffA);
;             PG8_WAIT_V(8); PG8_WAIT_L(0); PG8_BAR; PG8_MMA(1, 0, At, B0); PG8_MMA(1, 1, At, B1); PG8_BAR; PG8_SCHED;
;         }
	s_add_i32 s58, 0, 0x18000
	s_add_i32 s59, 0, 0x1c000
	v_add_u32_e32 v2, s58, v181
	v_add_u32_e32 v22, s59, v181
	ds_read_b128 v[10:13], v2
	ds_read_b128 v[14:17], v2 offset:512
	ds_read_b128 v[164:167], v2 offset:2048
	ds_read_b128 v[168:171], v2 offset:2560
	ds_read_b128 v[2:5], v22
	ds_read_b128 v[6:9], v22 offset:512
	ds_read_b128 v[18:21], v22 offset:2048
	ds_read_b128 v[22:25], v22 offset:2560
	s_add_u32 s36, s36, 0x80000
	s_addc_u32 s37, s37, 0
	s_mov_b32 m0, s41
	ds_read_b128 v[210:213], v185 offset:32768
	ds_read_b128 v[214:217], v185 offset:33280
	ds_read_b128 v[218:221], v185 offset:34816
	ds_read_b128 v[222:225], v185 offset:35328
	ds_read_b128 v[226:229], v185 offset:36864
	ds_read_b128 v[230:233], v185 offset:37376
	ds_read_b128 v[234:237], v185 offset:38912
	ds_read_b128 v[238:241], v185 offset:39424
	global_load_lds_dwordx4 v174, s[36:37]
	s_mov_b32 m0, s42
	s_nop 0
	global_load_lds_dwordx4 v178, s[36:37]
	s_waitcnt vmcnt(8)
	s_waitcnt lgkmcnt(0)
	s_barrier
	s_setprio 1
	s_waitcnt lgkmcnt(0)
	v_mfma_f32_16x16x128_f8f6f4 v[154:157], v[10:17], v[210:217], v[154:157]
	v_mfma_f32_16x16x128_f8f6f4 v[150:153], v[164:171], v[210:217], v[150:153]
	v_mfma_f32_16x16x128_f8f6f4 v[138:141], v[10:17], v[218:225], v[138:141]
	v_mfma_f32_16x16x128_f8f6f4 v[134:137], v[164:171], v[218:225], v[134:137]
	v_mfma_f32_16x16x128_f8f6f4 v[122:125], v[10:17], v[226:233], v[122:125]
	v_mfma_f32_16x16x128_f8f6f4 v[118:121], v[164:171], v[226:233], v[118:121]
	v_mfma_f32_16x16x128_f8f6f4 v[106:109], v[10:17], v[234:241], v[106:109]
	v_mfma_f32_16x16x128_f8f6f4 v[102:105], v[164:171], v[234:241], v[102:105]
	s_setprio 0
	s_setprio 1
	v_mfma_f32_16x16x128_f8f6f4 v[146:149], v[2:9], v[210:217], v[146:149]
	v_mfma_f32_16x16x128_f8f6f4 v[142:145], v[18:25], v[210:217], v[142:145]
	v_mfma_f32_16x16x128_f8f6f4 v[130:133], v[2:9], v[218:225], v[130:133]
	v_mfma_f32_16x16x128_f8f6f4 v[126:129], v[18:25], v[218:225], v[126:129]
	v_mfma_f32_16x16x128_f8f6f4 v[114:117], v[2:9], v[226:233], v[114:117]
	v_mfma_f32_16x16x128_f8f6f4 v[110:113], v[18:25], v[226:233], v[110:113]
	v_mfma_f32_16x16x128_f8f6f4 v[98:101], v[2:9], v[234:241], v[98:101]
	v_mfma_f32_16x16x128_f8f6f4 v[94:97], v[18:25], v[234:241], v[94:97]
	s_setprio 0
	s_barrier
	s_add_i32 s36, s58, s38
	s_add_i32 m0, s36, 0xffffff80
	ds_read_b128 v[210:213], v185 offset:49152
	ds_read_b128 v[214:217], v185 offset:49664
	ds_read_b128 v[218:221], v185 offset:51200
	ds_read_b128 v[222:225], v185 offset:51712
	ds_read_b128 v[226:229], v185 offset:53248
	ds_read_b128 v[230:233], v185 offset:53760
	ds_read_b128 v[234:237], v185 offset:55296
	ds_read_b128 v[238:241], v185 offset:55808
	global_load_lds_dwordx4 v176, s[34:35] offset:128
	s_add_i32 m0, s36, 0x2000
	s_add_u32 s34, s34, 0x80080
	v_lshl_add_u64 v[28:29], v[158:159], 0, s[12:13]
	s_addc_u32 s35, s35, 0
	s_add_i32 s36, s59, s38
	global_load_lds_dwordx4 v[28:29], off
	s_mov_b32 m0, s36
	s_nop 0
	global_load_lds_dwordx4 v176, s[34:35]
	s_add_i32 m0, s36, 0x2000
	s_nop 0
	global_load_lds_dwordx4 v188, s[34:35]
	v_lshl_add_u64 v[28:29], v[160:161], 0, s[12:13]
	s_mov_b32 m0, s46
	s_nop 0
	global_load_lds_dwordx4 v[28:29], off
	v_lshl_add_u64 v[28:29], v[162:163], 0, s[12:13]
	s_mov_b32 m0, s47
	s_nop 0
	global_load_lds_dwordx4 v[28:29], off
	s_waitcnt vmcnt(8)
	s_waitcnt lgkmcnt(0)
	s_barrier
	s_setprio 1
	s_waitcnt lgkmcnt(0)
	v_mfma_f32_16x16x128_f8f6f4 v[90:93], v[10:17], v[210:217], v[90:93]
	v_mfma_f32_16x16x128_f8f6f4 v[86:89], v[164:171], v[210:217], v[86:89]
	v_mfma_f32_16x16x128_f8f6f4 v[74:77], v[10:17], v[218:225], v[74:77]
	v_mfma_f32_16x16x128_f8f6f4 v[70:73], v[164:171], v[218:225], v[70:73]
	v_mfma_f32_16x16x128_f8f6f4 v[58:61], v[10:17], v[226:233], v[58:61]
	v_mfma_f32_16x16x128_f8f6f4 v[54:57], v[164:171], v[226:233], v[54:57]
	v_mfma_f32_16x16x128_f8f6f4 v[42:45], v[10:17], v[234:241], v[42:45]
	v_mfma_f32_16x16x128_f8f6f4 v[38:41], v[164:171], v[234:241], v[38:41]
	s_setprio 0
	s_setprio 1
	v_mfma_f32_16x16x128_f8f6f4 v[82:85], v[2:9], v[210:217], v[82:85]
	v_mfma_f32_16x16x128_f8f6f4 v[78:81], v[18:25], v[210:217], v[78:81]
	v_mfma_f32_16x16x128_f8f6f4 v[66:69], v[2:9], v[218:225], v[66:69]
	v_mfma_f32_16x16x128_f8f6f4 v[62:65], v[18:25], v[218:225], v[62:65]
	v_mfma_f32_16x16x128_f8f6f4 v[50:53], v[2:9], v[226:233], v[50:53]
	v_mfma_f32_16x16x128_f8f6f4 v[46:49], v[18:25], v[226:233], v[46:49]
	v_mfma_f32_16x16x128_f8f6f4 v[34:37], v[2:9], v[234:241], v[34:37]
	v_mfma_f32_16x16x128_f8f6f4 v[30:33], v[18:25], v[234:241], v[30:33]
	s_setprio 0
	s_barrier
	s_add_i32 s57, s57, 2
	s_add_u32 s30, s30, 0x100
	s_addc_u32 s31, s31, 0
	s_cmp_gt_u32 s57, 29
	s_cbranch_scc1 .LBB0_1711

; __device__ __forceinline__ unsigned xb_ld(unsigned* p)              { return __hip_atomic_load(p, __ATOMIC_RELAXED, __HIP_MEMORY_SCOPE_AGENT); }
; __device__ __forceinline__ unsigned xb_add(unsigned* p, unsigned v) { return __hip_atomic_fetch_add(p, v, __ATOMIC_RELAXED, __HIP_MEMORY_SCOPE_AGENT); }
; #define XB_SPIN(cond, bar) do { unsigned _sp = 0; while (cond) { __builtin_amdgcn_s_sleep(1); \
;     if ((++_sp & 255u) == 0u) { if (xb_ld(&(bar)[XB_TMO])) break; if (_sp > XB_SPIN_CAP) { atomicAdd(&(bar)[XB_TMO], 1u); break; } } } } while (0)
; __device__ __forceinline__ void xcd_barrier(const XcdBarrier& b) {
;     ...
;         const unsigned old = xb_add(&bar[XB_XSUB(b.x)], 1u);
;         const unsigned gen = old / nloc;
;         if (old + 1u == (gen + 1u) * nloc) {
;             __builtin_amdgcn_fence(__ATOMIC_RELEASE, "agent");
;             asm volatile("s_waitcnt vmcnt(0)" ::: "memory");
;             const unsigned og = xb_add(&bar[XB_TOP], 1u);
;             const unsigned tg = og / nx;
;             if (og + 1u == (tg + 1u) * nx) xb_add(&bar[XB_TOPGEN], 1u);
;             else XB_SPIN(xb_ld(&bar[XB_TOPGEN]) == tg, bar);
;             __builtin_amdgcn_fence(__ATOMIC_ACQUIRE, "agent");
;             xb_add(&bar[XB_XGEN(b.x)], 1u);
;             asm volatile("s_waitcnt vmcnt(0)" ::: "memory");
;         } else {
;             XB_SPIN(xb_ld(&bar[XB_XGEN(b.x)]) == gen, bar);
.LBB0_1883:
	s_or_b64 exec, exec, s[16:17]
	v_cvt_f32_u32_e32 v5, v3
	s_waitcnt vmcnt(0)
	v_readfirstlane_b32 s14, v4
	v_sub_u32_e32 v4, 0, v3
	v_rcp_iflag_f32_e32 v5, v5
	v_add_u32_e32 v6, s14, v2
	v_mul_f32_e32 v5, 0x4f7ffffe, v5
	v_cvt_u32_f32_e32 v5, v5
	v_mul_lo_u32 v2, v4, v5
	v_mul_hi_u32 v2, v5, v2
	v_add_u32_e32 v2, v5, v2
	v_mul_hi_u32 v2, v6, v2
	v_mul_lo_u32 v4, v2, v3
	v_sub_u32_e32 v4, v6, v4
	v_add_u32_e32 v5, 1, v2
	v_cmp_ge_u32_e32 vcc, v4, v3
	s_nop 1
	v_cndmask_b32_e32 v2, v2, v5, vcc
	v_sub_u32_e32 v5, v4, v3
	v_cndmask_b32_e32 v4, v4, v5, vcc
	v_add_u32_e32 v5, 1, v2
	v_cmp_ge_u32_e32 vcc, v4, v3
	v_add_u32_e32 v4, 1, v6
	s_nop 0
	v_cndmask_b32_e32 v2, v2, v5, vcc
	v_mul_lo_u32 v5, v3, v2
	v_add_u32_e32 v3, v5, v3
	v_cmp_ne_u32_e32 vcc, v4, v3
	s_and_saveexec_b64 s[14:15], vcc
	s_xor_b64 s[14:15], exec, s[14:15]
	s_cbranch_execz .LBB0_1897
	s_waitcnt lgkmcnt(0)
	buffer_inv sc1
	v_mov_b32_e32 v1, 0x2000
	global_load_dword v1, v1, s[10:11] offset:1024 sc1
	s_add_u32 s20, s10, 0x2400
	s_addc_u32 s21, s11, 0
	s_waitcnt vmcnt(0)
	v_cmp_eq_u32_e32 vcc, v1, v2
	s_and_saveexec_b64 s[16:17], vcc
	s_cbranch_execz .LBB0_1896
	v_readlane_b32 s18, v249, 11
	v_readlane_b32 s19, v249, 12
	s_add_u32 s18, s18, 0x4200
	s_addc_u32 s19, s19, 0
	s_mov_b32 s33, 1
	s_mov_b64 s[22:23], 0
	v_mov_b32_e32 v1, 0
	s_branch .LBB0_1887

; __device__ __forceinline__ unsigned xb_ld(unsigned* p)              { return __hip_atomic_load(p, __ATOMIC_RELAXED, __HIP_MEMORY_SCOPE_AGENT); }
; __device__ __forceinline__ unsigned xb_add(unsigned* p, unsigned v) { return __hip_atomic_fetch_add(p, v, __ATOMIC_RELAXED, __HIP_MEMORY_SCOPE_AGENT); }
; #define XB_SPIN(cond, bar) do { unsigned _sp = 0; while (cond) { __builtin_amdgcn_s_sleep(1); \
;     if ((++_sp & 255u) == 0u) { if (xb_ld(&(bar)[XB_TMO])) break; if (_sp > XB_SPIN_CAP) { atomicAdd(&(bar)[XB_TMO], 1u); break; } } } } while (0)
; __device__ __forceinline__ void xcd_barrier(const XcdBarrier& b) {
;     ...
;         if (old + 1u == (gen + 1u) * nloc) {
;             __builtin_amdgcn_fence(__ATOMIC_RELEASE, "agent");
;             asm volatile("s_waitcnt vmcnt(0)" ::: "memory");
;             const unsigned og = xb_add(&bar[XB_TOP], 1u);
;             const unsigned tg = og / nx;
;             if (og + 1u == (tg + 1u) * nx) xb_add(&bar[XB_TOPGEN], 1u);
;             else XB_SPIN(xb_ld(&bar[XB_TOPGEN]) == tg, bar);
;             __builtin_amdgcn_fence(__ATOMIC_ACQUIRE, "agent");
;             xb_add(&bar[XB_XGEN(b.x)], 1u);
;             asm volatile("s_waitcnt vmcnt(0)" ::: "memory");
;         } else {
;             XB_SPIN(xb_ld(&bar[XB_XGEN(b.x)]) == gen, bar);
;             __builtin_amdgcn_fence(__ATOMIC_ACQUIRE, "agent");
;             asm volatile("s_waitcnt vmcnt(0)" ::: "memory");
.LBB0_1896:
	s_or_b64 exec, exec, s[16:17]
	s_waitcnt vmcnt(0)
	s_waitcnt vmcnt(0)
.LBB0_1897:
	s_andn2_saveexec_b64 s[14:15], s[14:15]
	s_cbranch_execz .LBB0_1917
	s_mov_b64 s[14:15], exec
	buffer_wbl2 sc1
	s_waitcnt lgkmcnt(0)
	s_waitcnt vmcnt(0)
	buffer_inv sc1
	v_mbcnt_lo_u32_b32 v2, s14, 0
	v_mbcnt_hi_u32_b32 v2, s15, v2
	v_cmp_eq_u32_e32 vcc, 0, v2
	s_and_saveexec_b64 s[16:17], vcc
	s_cbranch_execz .LBB0_1900
	s_bcnt1_i32_b64 s14, s[14:15]
	v_mov_b32_e32 v4, s14
	v_readlane_b32 s14, v249, 11
	v_mov_b32_e32 v3, 0x7000
	v_readlane_b32 s15, v249, 12
	s_nop 4
	global_atomic_add v3, v3, v4, s[14:15] offset:1024 sc0

; __device__ __forceinline__ unsigned xb_ld(unsigned* p)              { return __hip_atomic_load(p, __ATOMIC_RELAXED, __HIP_MEMORY_SCOPE_AGENT); }
; __device__ __forceinline__ unsigned xb_add(unsigned* p, unsigned v) { return __hip_atomic_fetch_add(p, v, __ATOMIC_RELAXED, __HIP_MEMORY_SCOPE_AGENT); }
; #define XB_SPIN(cond, bar) do { unsigned _sp = 0; while (cond) { __builtin_amdgcn_s_sleep(1); \
;     if ((++_sp & 255u) == 0u) { if (xb_ld(&(bar)[XB_TMO])) break; if (_sp > XB_SPIN_CAP) { atomicAdd(&(bar)[XB_TMO], 1u); break; } } } } while (0)
; __device__ __forceinline__ void xcd_barrier(const XcdBarrier& b) {
;     ...
;             if (og + 1u == (tg + 1u) * nx) xb_add(&bar[XB_TOPGEN], 1u);
;             else XB_SPIN(xb_ld(&bar[XB_TOPGEN]) == tg, bar);
;             __builtin_amdgcn_fence(__ATOMIC_ACQUIRE, "agent");
;             xb_add(&bar[XB_XGEN(b.x)], 1u);
;             asm volatile("s_waitcnt vmcnt(0)" ::: "memory");
.LBB0_1914:
	s_or_b64 exec, exec, s[14:15]
	s_mov_b64 s[14:15], exec
	v_mbcnt_lo_u32_b32 v1, s14, 0
	v_mbcnt_hi_u32_b32 v1, s15, v1
	v_cmp_eq_u32_e32 vcc, 0, v1
	s_waitcnt vmcnt(0)
	s_and_saveexec_b64 s[16:17], vcc
	s_cbranch_execz .LBB0_1916
	s_bcnt1_i32_b64 s14, s[14:15]
	v_mov_b32_e32 v1, 0x2000
	v_mov_b32_e32 v2, s14
	global_atomic_add v1, v2, s[10:11] offset:1024

; #define PG8_STAGE(bufoff, gbase, voff) do { _Pragma("unroll") for (int _i = 0; _i < 2; ++_i) \
;         __builtin_amdgcn_global_load_lds((const unsigned*)((const char*)(gbase) + (voff)[_i]), (PG8_LAS unsigned*)(lds + (bufoff) + ldsw + _i * 8192), 16, 0, 0); } while (0)
; #define PG8_LDA(dst, b, h) do { _Pragma("unroll") for (int m = 0; m < 4; ++m) { const i32x4 _l = *(const PG8_LAS i32x4*)(lds + PG8_SA(b, h) + aoff + m * 2048), _h = *(const PG8_LAS i32x4*)(lds + PG8_SA(b, h) + aoff + m * 2048 + 512); dst[m] = PG8_CAT(_l, _h); } } while (0)
; #define PG8_LDB(dst, b, h) do { _Pragma("unroll") for (int n = 0; n < 2; ++n) { const i32x4 _l = *(const PG8_LAS i32x4*)(lds + PG8_SB(b, h) + boff + n * 2048), _h = *(const PG8_LAS i32x4*)(lds + PG8_SB(b, h) + boff + n * 2048 + 512); dst[n] = PG8_CAT(_l, _h); } } while (0)
; #define PG8_WAIT_V(n) asm volatile("s_waitcnt vmcnt(" #n ")" ::: "memory")
; #define PG8_WAIT_L(n) asm volatile("s_waitcnt lgkmcnt(" #n ")" ::: "memory")
; #define PG8_BAR __builtin_amdgcn_s_barrier()
; #define PG8_SCHED __builtin_amdgcn_sched_barrier(0)
;     ...
;         for (int t = 0; t < nt; t += 2) {
;             const bool last = (t == nt - 2);
;             const char* a1 = cA + (size_t)(t + 1) * kstep;
;             const char* a2 = last ? nA : cA + (size_t)(t + 2) * kstep; const char* b2 = last ? nB : cB + (size_t)(t + 2) * kstep;
;             const char* a3 = a2 + kstep; const char* b3 = b2 + kstep;
;             if (last && has_next) S.a_ready(nxt);
;             if constexpr (Epi::MIDK) { if (t == nt / 2) { if constexpr (ES == 1) asm volatile("s_nop 15\n\ts_nop 15" ::: "memory"); E.mid(acc, cur, wr, wc, fr, fq); } }
;             PG8_LDB(B0, 0, 0); PG8_LDB(B1, 0, 1); PG8_SCHED; PG8_LDA(At, 0, 0); PG8_STAGE(PG8_SA(1, 1), a1 + hstepA, voffA);
;             PG8_WAIT_V(8); PG8_WAIT_L(0); PG8_BAR; PG8_MMA(0, 0, At, B0); PG8_MMA(0, 1, At, B1); PG8_BAR; PG8_SCHED;
;             PG8_LDA(At, 0, 1); PG8_STAGE(PG8_SB(0, 0), b2, voffB); PG8_STAGE(PG8_SB(0, 1), b2 + hstepB, voffB); PG8_STAGE(PG8_SA(0, 0), a2, voffA);
;             PG8_WAIT_V(8); PG8_WAIT_L(0); PG8_BAR; PG8_MMA(1, 0, At, B0); PG8_MMA(1, 1, At, B1); PG8_BAR; PG8_SCHED;
.LBB0_2082:
	ds_read_b128 v[18:21], v185
	ds_read_b128 v[22:25], v185 offset:512
	ds_read_b128 v[26:29], v185 offset:2048
	ds_read_b128 v[30:33], v185 offset:2560
	ds_read_b128 v[2:5], v187
	ds_read_b128 v[6:9], v187 offset:512
	ds_read_b128 v[10:13], v187 offset:2048
	ds_read_b128 v[14:17], v187 offset:2560
	s_add_u32 s36, s34, 0x100
	s_addc_u32 s37, s35, 0
	s_cmp_eq_u32 s62, 28
	s_cselect_b32 s41, s25, s37
	s_cselect_b32 s40, s58, s36
	s_cselect_b32 s39, s23, s61
	s_cselect_b32 s38, s59, s60
	s_add_i32 m0, s42, 0xc000
	ds_read_b128 v[192:195], v190
	ds_read_b128 v[196:199], v190 offset:512
	ds_read_b128 v[200:203], v190 offset:2048
	ds_read_b128 v[204:207], v190 offset:2560
	ds_read_b128 v[208:211], v190 offset:4096
	ds_read_b128 v[212:215], v190 offset:4608
	ds_read_b128 v[216:219], v190 offset:6144
	ds_read_b128 v[220:223], v190 offset:6656
	global_load_lds_dwordx4 v166, s[34:35]
	s_add_i32 m0, s42, 0xe000
	s_nop 0
	global_load_lds_dwordx4 v168, s[34:35]
	s_waitcnt vmcnt(8)
	s_waitcnt lgkmcnt(0)
	s_barrier
	s_setprio 1
	s_waitcnt lgkmcnt(0)
	v_mfma_f32_16x16x128_f8f6f4 v[158:161], v[18:25], v[192:199], v[158:161]
	v_mfma_f32_16x16x128_f8f6f4 v[154:157], v[26:33], v[192:199], v[154:157]
	v_mfma_f32_16x16x128_f8f6f4 v[142:145], v[18:25], v[200:207], v[142:145]
	v_mfma_f32_16x16x128_f8f6f4 v[138:141], v[26:33], v[200:207], v[138:141]
	v_mfma_f32_16x16x128_f8f6f4 v[126:129], v[18:25], v[208:215], v[126:129]
	v_mfma_f32_16x16x128_f8f6f4 v[122:125], v[26:33], v[208:215], v[122:125]
	v_mfma_f32_16x16x128_f8f6f4 v[110:113], v[18:25], v[216:223], v[110:113]
	v_mfma_f32_16x16x128_f8f6f4 v[106:109], v[26:33], v[216:223], v[106:109]
	s_setprio 0
	s_setprio 1
	v_mfma_f32_16x16x128_f8f6f4 v[150:153], v[2:9], v[192:199], v[150:153]
	v_mfma_f32_16x16x128_f8f6f4 v[146:149], v[10:17], v[192:199], v[146:149]
	v_mfma_f32_16x16x128_f8f6f4 v[134:137], v[2:9], v[200:207], v[134:137]
	v_mfma_f32_16x16x128_f8f6f4 v[130:133], v[10:17], v[200:207], v[130:133]
	v_mfma_f32_16x16x128_f8f6f4 v[118:121], v[2:9], v[208:215], v[118:121]
	v_mfma_f32_16x16x128_f8f6f4 v[114:117], v[10:17], v[208:215], v[114:117]
	v_mfma_f32_16x16x128_f8f6f4 v[102:105], v[2:9], v[216:223], v[102:105]
	v_mfma_f32_16x16x128_f8f6f4 v[98:101], v[10:17], v[216:223], v[98:101]
	s_setprio 0
	s_barrier
	s_add_i32 s34, s54, s33
	s_mov_b32 m0, s34
	ds_read_b128 v[192:195], v190 offset:16384
	ds_read_b128 v[196:199], v190 offset:16896
	ds_read_b128 v[200:203], v190 offset:18432
	ds_read_b128 v[204:207], v190 offset:18944
	ds_read_b128 v[208:211], v190 offset:20480
	ds_read_b128 v[212:215], v190 offset:20992
	ds_read_b128 v[216:219], v190 offset:22528
	ds_read_b128 v[220:223], v190 offset:23040
	global_load_lds_dwordx4 v162, s[38:39]
	s_add_i32 m0, s34, 0x2000
	s_add_u32 s34, s38, 0x80000
	v_lshl_add_u64 v[176:177], s[38:39], 0, v[164:165]
	s_addc_u32 s35, s39, 0
	s_add_i32 s63, s55, s33
	global_load_lds_dwordx4 v164, s[38:39]
	s_mov_b32 m0, s63
	s_nop 0
	global_load_lds_dwordx4 v162, s[34:35]
	s_add_i32 m0, s63, 0x2000
	s_nop 0
	global_load_lds_dwordx4 v164, s[34:35]
	s_mov_b32 m0, s42
	s_nop 0
	global_load_lds_dwordx4 v162, s[40:41]
	s_mov_b32 m0, s43
	s_nop 0
	global_load_lds_dwordx4 v164, s[40:41]
	s_waitcnt vmcnt(8)
	s_waitcnt lgkmcnt(0)
	s_barrier
	s_setprio 1
	s_waitcnt lgkmcnt(0)
	v_mfma_f32_16x16x128_f8f6f4 v[94:97], v[18:25], v[192:199], v[94:97]
	v_mfma_f32_16x16x128_f8f6f4 v[90:93], v[26:33], v[192:199], v[90:93]
	v_mfma_f32_16x16x128_f8f6f4 v[78:81], v[18:25], v[200:207], v[78:81]
	v_mfma_f32_16x16x128_f8f6f4 v[74:77], v[26:33], v[200:207], v[74:77]
	v_mfma_f32_16x16x128_f8f6f4 v[62:65], v[18:25], v[208:215], v[62:65]
	v_mfma_f32_16x16x128_f8f6f4 v[58:61], v[26:33], v[208:215], v[58:61]
	v_mfma_f32_16x16x128_f8f6f4 v[54:57], v[18:25], v[216:223], v[54:57]
	v_mfma_f32_16x16x128_f8f6f4 v[42:45], v[26:33], v[216:223], v[42:45]
	s_setprio 0
	s_setprio 1
	v_mfma_f32_16x16x128_f8f6f4 v[86:89], v[2:9], v[192:199], v[86:89]
	v_mfma_f32_16x16x128_f8f6f4 v[82:85], v[10:17], v[192:199], v[82:85]
	v_mfma_f32_16x16x128_f8f6f4 v[70:73], v[2:9], v[200:207], v[70:73]
	v_mfma_f32_16x16x128_f8f6f4 v[66:69], v[10:17], v[200:207], v[66:69]
	v_mfma_f32_16x16x128_f8f6f4 v[50:53], v[2:9], v[208:215], v[50:53]
	v_mfma_f32_16x16x128_f8f6f4 v[46:49], v[10:17], v[208:215], v[46:49]
	v_mfma_f32_16x16x128_f8f6f4 v[38:41], v[2:9], v[216:223], v[38:41]
	v_mfma_f32_16x16x128_f8f6f4 v[34:37], v[10:17], v[216:223], v[34:37]
	s_setprio 0
	s_barrier
; #define PG8_STAGE(bufoff, gbase, voff) do { _Pragma("unroll") for (int _i = 0; _i < 2; ++_i) \
;         __builtin_amdgcn_global_load_lds((const unsigned*)((const char*)(gbase) + (voff)[_i]), (PG8_LAS unsigned*)(lds + (bufoff) + ldsw + _i * 8192), 16, 0, 0); } while (0)
; #define PG8_LDA(dst, b, h) do { _Pragma("unroll") for (int m = 0; m < 4; ++m) { const i32x4 _l = *(const PG8_LAS i32x4*)(lds + PG8_SA(b, h) + aoff + m * 2048), _h = *(const PG8_LAS i32x4*)(lds + PG8_SA(b, h) + aoff + m * 2048 + 512); dst[m] = PG8_CAT(_l, _h); } } while (0)
; #define PG8_LDB(dst, b, h) do { _Pragma("unroll") for (int n = 0; n < 2; ++n) { const i32x4 _l = *(const PG8_LAS i32x4*)(lds + PG8_SB(b, h) + boff + n * 2048), _h = *(const PG8_LAS i32x4*)(lds + PG8_SB(b, h) + boff + n * 2048 + 512); dst[n] = PG8_CAT(_l, _h); } } while (0)
; #define PG8_WAIT_V(n) asm volatile("s_waitcnt vmcnt(" #n ")" ::: "memory")
; #define PG8_WAIT_L(n) asm volatile("s_waitcnt lgkmcnt(" #n ")" ::: "memory")
; #define PG8_BAR __builtin_amdgcn_s_barrier()
; #define PG8_SCHED __builtin_amdgcn_sched_barrier(0)
;     ...
;             PG8_LDB(B0, 1, 0); PG8_LDB(B1, 1, 1); PG8_SCHED; PG8_LDA(At, 1, 0); PG8_STAGE(PG8_SA(0, 1), a2 + hstepA, voffA);
;             PG8_WAIT_V(8); PG8_WAIT_L(0); PG8_BAR; PG8_MMA(0, 0, At, B0); PG8_MMA(0, 1, At, B1); PG8_BAR; PG8_SCHED;
;             PG8_LDA(At, 1, 1); PG8_STAGE(PG8_SB(1, 0), b3, voffB); PG8_STAGE(PG8_SB(1, 1), b3 + hstepB, voffB); PG8_STAGE(PG8_SA(1, 0), a3, voffA);
;             PG8_WAIT_V(8); PG8_WAIT_L(0); PG8_BAR; PG8_MMA(1, 0, At, B0); PG8_MMA(1, 1, At, B1); PG8_BAR; PG8_SCHED;
;         }
	s_add_i32 s63, 0, 0x18000
	s_add_i32 s64, 0, 0x1c000
	v_add_u32_e32 v14, s63, v181
	v_add_u32_e32 v30, s64, v181
	ds_read_b128 v[2:5], v14
	ds_read_b128 v[6:9], v14 offset:512
	ds_read_b128 v[10:13], v14 offset:2048
	ds_read_b128 v[14:17], v14 offset:2560
	ds_read_b128 v[18:21], v30
	ds_read_b128 v[22:25], v30 offset:512
	ds_read_b128 v[26:29], v30 offset:2048
	ds_read_b128 v[30:33], v30 offset:2560
	s_add_u32 s34, s40, 0x80000
	s_addc_u32 s35, s41, 0
	s_mov_b32 m0, s46
	ds_read_b128 v[192:195], v190 offset:32768
	ds_read_b128 v[196:199], v190 offset:33280
	ds_read_b128 v[200:203], v190 offset:34816
	ds_read_b128 v[204:207], v190 offset:35328
	ds_read_b128 v[208:211], v190 offset:36864
	ds_read_b128 v[212:215], v190 offset:37376
	ds_read_b128 v[216:219], v190 offset:38912
	ds_read_b128 v[220:223], v190 offset:39424
	global_load_lds_dwordx4 v162, s[34:35]
	s_mov_b32 m0, s47
	s_nop 0
	global_load_lds_dwordx4 v164, s[34:35]
	s_waitcnt vmcnt(8)
	s_waitcnt lgkmcnt(0)
	s_barrier
	s_setprio 1
	s_waitcnt lgkmcnt(0)
	v_mfma_f32_16x16x128_f8f6f4 v[158:161], v[2:9], v[192:199], v[158:161]
	v_mfma_f32_16x16x128_f8f6f4 v[154:157], v[10:17], v[192:199], v[154:157]
	v_mfma_f32_16x16x128_f8f6f4 v[142:145], v[2:9], v[200:207], v[142:145]
	v_mfma_f32_16x16x128_f8f6f4 v[138:141], v[10:17], v[200:207], v[138:141]
	v_mfma_f32_16x16x128_f8f6f4 v[126:129], v[2:9], v[208:215], v[126:129]
	v_mfma_f32_16x16x128_f8f6f4 v[122:125], v[10:17], v[208:215], v[122:125]
	v_mfma_f32_16x16x128_f8f6f4 v[110:113], v[2:9], v[216:223], v[110:113]
	v_mfma_f32_16x16x128_f8f6f4 v[106:109], v[10:17], v[216:223], v[106:109]
	s_setprio 0
	s_setprio 1
	v_mfma_f32_16x16x128_f8f6f4 v[150:153], v[18:25], v[192:199], v[150:153]
	v_mfma_f32_16x16x128_f8f6f4 v[146:149], v[26:33], v[192:199], v[146:149]
	v_mfma_f32_16x16x128_f8f6f4 v[134:137], v[18:25], v[200:207], v[134:137]
	v_mfma_f32_16x16x128_f8f6f4 v[130:133], v[26:33], v[200:207], v[130:133]
	v_mfma_f32_16x16x128_f8f6f4 v[118:121], v[18:25], v[208:215], v[118:121]
	v_mfma_f32_16x16x128_f8f6f4 v[114:117], v[26:33], v[208:215], v[114:117]
	v_mfma_f32_16x16x128_f8f6f4 v[102:105], v[18:25], v[216:223], v[102:105]
	v_mfma_f32_16x16x128_f8f6f4 v[98:101], v[26:33], v[216:223], v[98:101]
	s_setprio 0
	s_barrier
	s_add_i32 s34, s63, s33
	s_add_i32 m0, s34, 0xffffff80
	ds_read_b128 v[192:195], v190 offset:49152
	ds_read_b128 v[196:199], v190 offset:49664
	ds_read_b128 v[200:203], v190 offset:51200
	ds_read_b128 v[204:207], v190 offset:51712
	ds_read_b128 v[208:211], v190 offset:53248
	ds_read_b128 v[212:215], v190 offset:53760
	ds_read_b128 v[216:219], v190 offset:55296
	ds_read_b128 v[220:223], v190 offset:55808
	global_load_lds_dwordx4 v162, s[38:39] offset:128
	s_add_i32 m0, s34, 0x2000
	s_add_u32 s34, s38, 0x80080
	v_lshl_add_u64 v[174:175], v[176:177], 0, s[8:9]
	s_addc_u32 s35, s39, 0
	s_add_i32 s38, s64, s33
	global_load_lds_dwordx4 v[174:175], off
	s_mov_b32 m0, s38
	s_nop 0
	global_load_lds_dwordx4 v162, s[34:35]
	s_add_i32 m0, s38, 0x2000
	s_nop 0
	global_load_lds_dwordx4 v164, s[34:35]
	s_add_i32 m0, s51, 0xffffff80
	s_nop 0
	global_load_lds_dwordx4 v162, s[40:41] offset:128
	s_add_i32 m0, s52, 0xffffff80
	s_nop 0
	global_load_lds_dwordx4 v164, s[40:41] offset:128
	s_waitcnt vmcnt(8)
	s_waitcnt lgkmcnt(0)
	s_barrier
	s_setprio 1
	s_waitcnt lgkmcnt(0)
	v_mfma_f32_16x16x128_f8f6f4 v[94:97], v[2:9], v[192:199], v[94:97]
	v_mfma_f32_16x16x128_f8f6f4 v[90:93], v[10:17], v[192:199], v[90:93]
	v_mfma_f32_16x16x128_f8f6f4 v[78:81], v[2:9], v[200:207], v[78:81]
	v_mfma_f32_16x16x128_f8f6f4 v[74:77], v[10:17], v[200:207], v[74:77]
	v_mfma_f32_16x16x128_f8f6f4 v[62:65], v[2:9], v[208:215], v[62:65]
	v_mfma_f32_16x16x128_f8f6f4 v[58:61], v[10:17], v[208:215], v[58:61]
	v_mfma_f32_16x16x128_f8f6f4 v[54:57], v[2:9], v[216:223], v[54:57]
	v_mfma_f32_16x16x128_f8f6f4 v[42:45], v[10:17], v[216:223], v[42:45]
	s_setprio 0
	s_setprio 1
	v_mfma_f32_16x16x128_f8f6f4 v[86:89], v[18:25], v[192:199], v[86:89]
	v_mfma_f32_16x16x128_f8f6f4 v[82:85], v[26:33], v[192:199], v[82:85]
	v_mfma_f32_16x16x128_f8f6f4 v[70:73], v[18:25], v[200:207], v[70:73]
	v_mfma_f32_16x16x128_f8f6f4 v[66:69], v[26:33], v[200:207], v[66:69]
	v_mfma_f32_16x16x128_f8f6f4 v[50:53], v[18:25], v[208:215], v[50:53]
	v_mfma_f32_16x16x128_f8f6f4 v[46:49], v[26:33], v[208:215], v[46:49]
	v_mfma_f32_16x16x128_f8f6f4 v[38:41], v[18:25], v[216:223], v[38:41]
	v_mfma_f32_16x16x128_f8f6f4 v[34:37], v[26:33], v[216:223], v[34:37]
	s_setprio 0
	s_barrier
	s_add_i32 s62, s62, 2
	s_add_u32 s60, s60, 0x100
	s_addc_u32 s61, s61, 0
	s_cmp_gt_u32 s62, 29
	s_mov_b64 s[34:35], s[36:37]
	s_cbranch_scc0 .LBB0_2082
	s_and_b64 vcc, exec, s[16:17]
	s_cbranch_vccz .LBB0_2085
	s_barrier

; __device__ __forceinline__ unsigned xb_ld(unsigned* p)              { return __hip_atomic_load(p, __ATOMIC_RELAXED, __HIP_MEMORY_SCOPE_AGENT); }
; __device__ __forceinline__ unsigned xb_add(unsigned* p, unsigned v) { return __hip_atomic_fetch_add(p, v, __ATOMIC_RELAXED, __HIP_MEMORY_SCOPE_AGENT); }
; #define XB_SPIN(cond, bar) do { unsigned _sp = 0; while (cond) { __builtin_amdgcn_s_sleep(1); \
;     if ((++_sp & 255u) == 0u) { if (xb_ld(&(bar)[XB_TMO])) break; if (_sp > XB_SPIN_CAP) { atomicAdd(&(bar)[XB_TMO], 1u); break; } } } } while (0)
; __device__ __forceinline__ void xcd_barrier(const XcdBarrier& b) {
;     ...
;         const unsigned old = xb_add(&bar[XB_XSUB(b.x)], 1u);
;         const unsigned gen = old / nloc;
;         if (old + 1u == (gen + 1u) * nloc) {
;             __builtin_amdgcn_fence(__ATOMIC_RELEASE, "agent");
;             asm volatile("s_waitcnt vmcnt(0)" ::: "memory");
;             const unsigned og = xb_add(&bar[XB_TOP], 1u);
;             const unsigned tg = og / nx;
;             if (og + 1u == (tg + 1u) * nx) xb_add(&bar[XB_TOPGEN], 1u);
;             else XB_SPIN(xb_ld(&bar[XB_TOPGEN]) == tg, bar);
;             __builtin_amdgcn_fence(__ATOMIC_ACQUIRE, "agent");
;             xb_add(&bar[XB_XGEN(b.x)], 1u);
;             asm volatile("s_waitcnt vmcnt(0)" ::: "memory");
;         } else {
;             XB_SPIN(xb_ld(&bar[XB_XGEN(b.x)]) == gen, bar);
.LBB0_2254:
	s_or_b64 exec, exec, s[10:11]
	v_cvt_f32_u32_e32 v5, v3
	s_waitcnt vmcnt(0)
	v_readfirstlane_b32 s8, v4
	v_sub_u32_e32 v4, 0, v3
	v_rcp_iflag_f32_e32 v5, v5
	v_add_u32_e32 v6, s8, v2
	v_mul_f32_e32 v5, 0x4f7ffffe, v5
	v_cvt_u32_f32_e32 v5, v5
	v_mul_lo_u32 v2, v4, v5
	v_mul_hi_u32 v2, v5, v2
	v_add_u32_e32 v2, v5, v2
	v_mul_hi_u32 v2, v6, v2
	v_mul_lo_u32 v4, v2, v3
	v_sub_u32_e32 v4, v6, v4
	v_add_u32_e32 v5, 1, v2
	v_cmp_ge_u32_e32 vcc, v4, v3
	s_nop 1
	v_cndmask_b32_e32 v2, v2, v5, vcc
	v_sub_u32_e32 v5, v4, v3
	v_cndmask_b32_e32 v4, v4, v5, vcc
	v_add_u32_e32 v5, 1, v2
	v_cmp_ge_u32_e32 vcc, v4, v3
	v_add_u32_e32 v4, 1, v6
	s_nop 0
	v_cndmask_b32_e32 v2, v2, v5, vcc
	v_mul_lo_u32 v5, v3, v2
	v_add_u32_e32 v3, v5, v3
	v_cmp_ne_u32_e32 vcc, v4, v3
	s_and_saveexec_b64 s[8:9], vcc
	s_xor_b64 s[8:9], exec, s[8:9]
	s_cbranch_execz .LBB0_2268
	s_waitcnt lgkmcnt(0)
	buffer_inv sc1
	v_mov_b32_e32 v1, 0x2000
	global_load_dword v1, v1, s[6:7] offset:1024 sc1
	s_add_u32 s14, s6, 0x2400
	s_addc_u32 s15, s7, 0
	s_waitcnt vmcnt(0)
	v_cmp_eq_u32_e32 vcc, v1, v2
	s_and_saveexec_b64 s[10:11], vcc
	s_cbranch_execz .LBB0_2267
	v_readlane_b32 s12, v249, 11
	v_readlane_b32 s13, v249, 12
	s_add_u32 s12, s12, 0x4200
	s_addc_u32 s13, s13, 0
	s_mov_b32 s26, 1
	s_mov_b64 s[16:17], 0
	v_mov_b32_e32 v1, 0
	s_branch .LBB0_2258

; __device__ __forceinline__ unsigned xb_ld(unsigned* p)              { return __hip_atomic_load(p, __ATOMIC_RELAXED, __HIP_MEMORY_SCOPE_AGENT); }
; __device__ __forceinline__ unsigned xb_add(unsigned* p, unsigned v) { return __hip_atomic_fetch_add(p, v, __ATOMIC_RELAXED, __HIP_MEMORY_SCOPE_AGENT); }
; #define XB_SPIN(cond, bar) do { unsigned _sp = 0; while (cond) { __builtin_amdgcn_s_sleep(1); \
;     if ((++_sp & 255u) == 0u) { if (xb_ld(&(bar)[XB_TMO])) break; if (_sp > XB_SPIN_CAP) { atomicAdd(&(bar)[XB_TMO], 1u); break; } } } } while (0)
; __device__ __forceinline__ void xcd_barrier(const XcdBarrier& b) {
;     ...
;         if (old + 1u == (gen + 1u) * nloc) {
;             __builtin_amdgcn_fence(__ATOMIC_RELEASE, "agent");
;             asm volatile("s_waitcnt vmcnt(0)" ::: "memory");
;             const unsigned og = xb_add(&bar[XB_TOP], 1u);
;             const unsigned tg = og / nx;
;             if (og + 1u == (tg + 1u) * nx) xb_add(&bar[XB_TOPGEN], 1u);
;             else XB_SPIN(xb_ld(&bar[XB_TOPGEN]) == tg, bar);
;             __builtin_amdgcn_fence(__ATOMIC_ACQUIRE, "agent");
;             xb_add(&bar[XB_XGEN(b.x)], 1u);
;             asm volatile("s_waitcnt vmcnt(0)" ::: "memory");
;         } else {
;             XB_SPIN(xb_ld(&bar[XB_XGEN(b.x)]) == gen, bar);
;             __builtin_amdgcn_fence(__ATOMIC_ACQUIRE, "agent");
;             asm volatile("s_waitcnt vmcnt(0)" ::: "memory");
.LBB0_2267:
	s_or_b64 exec, exec, s[10:11]
	s_waitcnt vmcnt(0)
	s_waitcnt vmcnt(0)
.LBB0_2268:
	s_andn2_saveexec_b64 s[8:9], s[8:9]
	s_cbranch_execz .LBB0_2288
	s_mov_b64 s[8:9], exec
	buffer_wbl2 sc1
	s_waitcnt lgkmcnt(0)
	s_waitcnt vmcnt(0)
	buffer_inv sc1
	v_mbcnt_lo_u32_b32 v2, s8, 0
	v_mbcnt_hi_u32_b32 v2, s9, v2
	v_cmp_eq_u32_e32 vcc, 0, v2
	s_and_saveexec_b64 s[10:11], vcc
	s_cbranch_execz .LBB0_2271
	s_bcnt1_i32_b64 s8, s[8:9]
	v_mov_b32_e32 v4, s8
	v_readlane_b32 s8, v249, 11
	v_mov_b32_e32 v3, 0x7000
	v_readlane_b32 s9, v249, 12
	s_nop 4
	global_atomic_add v3, v3, v4, s[8:9] offset:1024 sc0

; __device__ __forceinline__ unsigned xb_ld(unsigned* p)              { return __hip_atomic_load(p, __ATOMIC_RELAXED, __HIP_MEMORY_SCOPE_AGENT); }
; __device__ __forceinline__ unsigned xb_add(unsigned* p, unsigned v) { return __hip_atomic_fetch_add(p, v, __ATOMIC_RELAXED, __HIP_MEMORY_SCOPE_AGENT); }
; #define XB_SPIN(cond, bar) do { unsigned _sp = 0; while (cond) { __builtin_amdgcn_s_sleep(1); \
;     if ((++_sp & 255u) == 0u) { if (xb_ld(&(bar)[XB_TMO])) break; if (_sp > XB_SPIN_CAP) { atomicAdd(&(bar)[XB_TMO], 1u); break; } } } } while (0)
; __device__ __forceinline__ void xcd_barrier(const XcdBarrier& b) {
;     ...
;             if (og + 1u == (tg + 1u) * nx) xb_add(&bar[XB_TOPGEN], 1u);
;             else XB_SPIN(xb_ld(&bar[XB_TOPGEN]) == tg, bar);
;             __builtin_amdgcn_fence(__ATOMIC_ACQUIRE, "agent");
;             xb_add(&bar[XB_XGEN(b.x)], 1u);
;             asm volatile("s_waitcnt vmcnt(0)" ::: "memory");
.LBB0_2285:
	s_or_b64 exec, exec, s[8:9]
	s_mov_b64 s[8:9], exec
	v_mbcnt_lo_u32_b32 v1, s8, 0
	v_mbcnt_hi_u32_b32 v1, s9, v1
	v_cmp_eq_u32_e32 vcc, 0, v1
	s_waitcnt vmcnt(0)
	s_and_saveexec_b64 s[10:11], vcc
	s_cbranch_execz .LBB0_2287
	s_bcnt1_i32_b64 s8, s[8:9]
	v_mov_b32_e32 v1, 0x2000
	v_mov_b32_e32 v2, s8
	global_atomic_add v1, v2, s[6:7] offset:1024

; #define PG8_STAGE(bufoff, gbase, voff) do { _Pragma("unroll") for (int _i = 0; _i < 2; ++_i) \
;         __builtin_amdgcn_global_load_lds((const unsigned*)((const char*)(gbase) + (voff)[_i]), (PG8_LAS unsigned*)(lds + (bufoff) + ldsw + _i * 8192), 16, 0, 0); } while (0)
; #define PG8_LDA(dst, b, h) do { _Pragma("unroll") for (int m = 0; m < 4; ++m) { const i32x4 _l = *(const PG8_LAS i32x4*)(lds + PG8_SA(b, h) + aoff + m * 2048), _h = *(const PG8_LAS i32x4*)(lds + PG8_SA(b, h) + aoff + m * 2048 + 512); dst[m] = PG8_CAT(_l, _h); } } while (0)
; #define PG8_LDB(dst, b, h) do { _Pragma("unroll") for (int n = 0; n < 2; ++n) { const i32x4 _l = *(const PG8_LAS i32x4*)(lds + PG8_SB(b, h) + boff + n * 2048), _h = *(const PG8_LAS i32x4*)(lds + PG8_SB(b, h) + boff + n * 2048 + 512); dst[n] = PG8_CAT(_l, _h); } } while (0)
; #define PG8_WAIT_V(n) asm volatile("s_waitcnt vmcnt(" #n ")" ::: "memory")
; #define PG8_WAIT_L(n) asm volatile("s_waitcnt lgkmcnt(" #n ")" ::: "memory")
; #define PG8_BAR __builtin_amdgcn_s_barrier()
; #define PG8_SCHED __builtin_amdgcn_sched_barrier(0)
;     ...
;         for (int t = 0; t < nt; t += 2) {
;             const bool last = (t == nt - 2);
;             const char* a1 = cA + (size_t)(t + 1) * kstep;
;             const char* a2 = last ? nA : cA + (size_t)(t + 2) * kstep; const char* b2 = last ? nB : cB + (size_t)(t + 2) * kstep;
;             const char* a3 = a2 + kstep; const char* b3 = b2 + kstep;
;             if (last && has_next) S.a_ready(nxt);
;             if constexpr (Epi::MIDK) { if (t == nt / 2) { if constexpr (ES == 1) asm volatile("s_nop 15\n\ts_nop 15" ::: "memory"); E.mid(acc, cur, wr, wc, fr, fq); } }
;             PG8_LDB(B0, 0, 0); PG8_LDB(B1, 0, 1); PG8_SCHED; PG8_LDA(At, 0, 0); PG8_STAGE(PG8_SA(1, 1), a1 + hstepA, voffA);
;             PG8_WAIT_V(8); PG8_WAIT_L(0); PG8_BAR; PG8_MMA(0, 0, At, B0); PG8_MMA(0, 1, At, B1); PG8_BAR; PG8_SCHED;
;             PG8_LDA(At, 0, 1); PG8_STAGE(PG8_SB(0, 0), b2, voffB); PG8_STAGE(PG8_SB(0, 1), b2 + hstepB, voffB); PG8_STAGE(PG8_SA(0, 0), a2, voffA);
;             PG8_WAIT_V(8); PG8_WAIT_L(0); PG8_BAR; PG8_MMA(1, 0, At, B0); PG8_MMA(1, 1, At, B1); PG8_BAR; PG8_SCHED;
.LBB0_2358:
	ds_read_b128 v[18:21], v190
	ds_read_b128 v[22:25], v190 offset:512
	ds_read_b128 v[26:29], v190 offset:2048
	ds_read_b128 v[30:33], v190 offset:2560
	ds_read_b128 v[2:5], v191
	ds_read_b128 v[6:9], v191 offset:512
	ds_read_b128 v[10:13], v191 offset:2048
	ds_read_b128 v[14:17], v191 offset:2560
	s_add_u32 s26, s24, 0x100
	s_addc_u32 s27, s25, 0
	s_cmp_eq_u32 s52, 28
	s_cselect_b32 s31, s17, s27
	s_cselect_b32 s30, s48, s26
	s_cselect_b32 s29, s15, s51
	s_cselect_b32 s28, s49, s50
	s_add_i32 m0, s23, 0xc000
	ds_read_b128 v[194:197], v192
	ds_read_b128 v[198:201], v192 offset:512
	ds_read_b128 v[202:205], v192 offset:2048
	ds_read_b128 v[206:209], v192 offset:2560
	ds_read_b128 v[210:213], v192 offset:4096
	ds_read_b128 v[214:217], v192 offset:4608
	ds_read_b128 v[218:221], v192 offset:6144
	ds_read_b128 v[222:225], v192 offset:6656
	global_load_lds_dwordx4 v170, s[24:25]
	s_add_i32 m0, s23, 0xe000
	s_nop 0
	global_load_lds_dwordx4 v172, s[24:25]
	s_waitcnt vmcnt(8)
	s_waitcnt lgkmcnt(0)
	s_barrier
	s_setprio 1
	s_waitcnt lgkmcnt(0)
	v_mfma_f32_16x16x128_f8f6f4 v[158:161], v[18:25], v[194:201], v[158:161]
	v_mfma_f32_16x16x128_f8f6f4 v[154:157], v[26:33], v[194:201], v[154:157]
	v_mfma_f32_16x16x128_f8f6f4 v[146:149], v[18:25], v[202:209], v[146:149]
	v_mfma_f32_16x16x128_f8f6f4 v[138:141], v[26:33], v[202:209], v[138:141]
	v_mfma_f32_16x16x128_f8f6f4 v[130:133], v[18:25], v[210:217], v[130:133]
	v_mfma_f32_16x16x128_f8f6f4 v[122:125], v[26:33], v[210:217], v[122:125]
	v_mfma_f32_16x16x128_f8f6f4 v[114:117], v[18:25], v[218:225], v[114:117]
	v_mfma_f32_16x16x128_f8f6f4 v[106:109], v[26:33], v[218:225], v[106:109]
	s_setprio 0
	s_setprio 1
	v_mfma_f32_16x16x128_f8f6f4 v[150:153], v[2:9], v[194:201], v[150:153]
	v_mfma_f32_16x16x128_f8f6f4 v[142:145], v[10:17], v[194:201], v[142:145]
	v_mfma_f32_16x16x128_f8f6f4 v[134:137], v[2:9], v[202:209], v[134:137]
	v_mfma_f32_16x16x128_f8f6f4 v[126:129], v[10:17], v[202:209], v[126:129]
	v_mfma_f32_16x16x128_f8f6f4 v[118:121], v[2:9], v[210:217], v[118:121]
	v_mfma_f32_16x16x128_f8f6f4 v[110:113], v[10:17], v[210:217], v[110:113]
	v_mfma_f32_16x16x128_f8f6f4 v[102:105], v[2:9], v[218:225], v[102:105]
	v_mfma_f32_16x16x128_f8f6f4 v[98:101], v[10:17], v[218:225], v[98:101]
	s_setprio 0
	s_barrier
	s_add_i32 s24, s42, s13
	s_mov_b32 m0, s24
	ds_read_b128 v[194:197], v192 offset:16384
	ds_read_b128 v[198:201], v192 offset:16896
	ds_read_b128 v[202:205], v192 offset:18432
	ds_read_b128 v[206:209], v192 offset:18944
	ds_read_b128 v[210:213], v192 offset:20480
	ds_read_b128 v[214:217], v192 offset:20992
	ds_read_b128 v[218:221], v192 offset:22528
	ds_read_b128 v[222:225], v192 offset:23040
	global_load_lds_dwordx4 v166, s[28:29]
	s_add_i32 m0, s24, 0x2000
	s_add_u32 s24, s28, 0x80000
	v_lshl_add_u64 v[182:183], s[28:29], 0, v[162:163]
	s_addc_u32 s25, s29, 0
	s_add_i32 s53, s43, s13
	global_load_lds_dwordx4 v162, s[28:29]
	s_mov_b32 m0, s53
	s_nop 0
	global_load_lds_dwordx4 v166, s[24:25]
	s_add_i32 m0, s53, 0x2000
	s_nop 0
	global_load_lds_dwordx4 v162, s[24:25]
	s_mov_b32 m0, s23
	s_nop 0
	global_load_lds_dwordx4 v168, s[30:31]
	s_mov_b32 m0, s35
	s_nop 0
	global_load_lds_dwordx4 v164, s[30:31]
	s_waitcnt vmcnt(8)
	s_waitcnt lgkmcnt(0)
	s_barrier
	s_setprio 1
	s_waitcnt lgkmcnt(0)
	v_mfma_f32_16x16x128_f8f6f4 v[94:97], v[18:25], v[194:201], v[94:97]
	v_mfma_f32_16x16x128_f8f6f4 v[90:93], v[26:33], v[194:201], v[90:93]
	v_mfma_f32_16x16x128_f8f6f4 v[82:85], v[18:25], v[202:209], v[82:85]
	v_mfma_f32_16x16x128_f8f6f4 v[74:77], v[26:33], v[202:209], v[74:77]
	v_mfma_f32_16x16x128_f8f6f4 v[66:69], v[18:25], v[210:217], v[66:69]
	v_mfma_f32_16x16x128_f8f6f4 v[58:61], v[26:33], v[210:217], v[58:61]
	v_mfma_f32_16x16x128_f8f6f4 v[50:53], v[18:25], v[218:225], v[50:53]
	v_mfma_f32_16x16x128_f8f6f4 v[42:45], v[26:33], v[218:225], v[42:45]
	s_setprio 0
	s_setprio 1
	v_mfma_f32_16x16x128_f8f6f4 v[86:89], v[2:9], v[194:201], v[86:89]
	v_mfma_f32_16x16x128_f8f6f4 v[78:81], v[10:17], v[194:201], v[78:81]
	v_mfma_f32_16x16x128_f8f6f4 v[70:73], v[2:9], v[202:209], v[70:73]
	v_mfma_f32_16x16x128_f8f6f4 v[62:65], v[10:17], v[202:209], v[62:65]
	v_mfma_f32_16x16x128_f8f6f4 v[54:57], v[2:9], v[210:217], v[54:57]
	v_mfma_f32_16x16x128_f8f6f4 v[46:49], v[10:17], v[210:217], v[46:49]
	v_mfma_f32_16x16x128_f8f6f4 v[38:41], v[2:9], v[218:225], v[38:41]
	v_mfma_f32_16x16x128_f8f6f4 v[34:37], v[10:17], v[218:225], v[34:37]
	s_setprio 0
	s_barrier
; #define PG8_STAGE(bufoff, gbase, voff) do { _Pragma("unroll") for (int _i = 0; _i < 2; ++_i) \
;         __builtin_amdgcn_global_load_lds((const unsigned*)((const char*)(gbase) + (voff)[_i]), (PG8_LAS unsigned*)(lds + (bufoff) + ldsw + _i * 8192), 16, 0, 0); } while (0)
; #define PG8_LDA(dst, b, h) do { _Pragma("unroll") for (int m = 0; m < 4; ++m) { const i32x4 _l = *(const PG8_LAS i32x4*)(lds + PG8_SA(b, h) + aoff + m * 2048), _h = *(const PG8_LAS i32x4*)(lds + PG8_SA(b, h) + aoff + m * 2048 + 512); dst[m] = PG8_CAT(_l, _h); } } while (0)
; #define PG8_LDB(dst, b, h) do { _Pragma("unroll") for (int n = 0; n < 2; ++n) { const i32x4 _l = *(const PG8_LAS i32x4*)(lds + PG8_SB(b, h) + boff + n * 2048), _h = *(const PG8_LAS i32x4*)(lds + PG8_SB(b, h) + boff + n * 2048 + 512); dst[n] = PG8_CAT(_l, _h); } } while (0)
; #define PG8_WAIT_V(n) asm volatile("s_waitcnt vmcnt(" #n ")" ::: "memory")
; #define PG8_WAIT_L(n) asm volatile("s_waitcnt lgkmcnt(" #n ")" ::: "memory")
; #define PG8_BAR __builtin_amdgcn_s_barrier()
; #define PG8_SCHED __builtin_amdgcn_sched_barrier(0)
;     ...
;             PG8_LDB(B0, 1, 0); PG8_LDB(B1, 1, 1); PG8_SCHED; PG8_LDA(At, 1, 0); PG8_STAGE(PG8_SA(0, 1), a2 + hstepA, voffA);
;             PG8_WAIT_V(8); PG8_WAIT_L(0); PG8_BAR; PG8_MMA(0, 0, At, B0); PG8_MMA(0, 1, At, B1); PG8_BAR; PG8_SCHED;
;             PG8_LDA(At, 1, 1); PG8_STAGE(PG8_SB(1, 0), b3, voffB); PG8_STAGE(PG8_SB(1, 1), b3 + hstepB, voffB); PG8_STAGE(PG8_SA(1, 0), a3, voffA);
;             PG8_WAIT_V(8); PG8_WAIT_L(0); PG8_BAR; PG8_MMA(1, 0, At, B0); PG8_MMA(1, 1, At, B1); PG8_BAR; PG8_SCHED;
;         }
	s_add_i32 s53, 0, 0x18000
	s_add_i32 s54, 0, 0x1c000
	v_add_u32_e32 v14, s53, v188
	v_add_u32_e32 v30, s54, v188
	ds_read_b128 v[2:5], v14
	ds_read_b128 v[6:9], v14 offset:512
	ds_read_b128 v[10:13], v14 offset:2048
	ds_read_b128 v[14:17], v14 offset:2560
	ds_read_b128 v[18:21], v30
	ds_read_b128 v[22:25], v30 offset:512
	ds_read_b128 v[26:29], v30 offset:2048
	ds_read_b128 v[30:33], v30 offset:2560
	s_add_u32 s24, s30, 0x80000
	s_addc_u32 s25, s31, 0
	s_mov_b32 m0, s36
	ds_read_b128 v[194:197], v192 offset:32768
	ds_read_b128 v[198:201], v192 offset:33280
	ds_read_b128 v[202:205], v192 offset:34816
	ds_read_b128 v[206:209], v192 offset:35328
	ds_read_b128 v[210:213], v192 offset:36864
	ds_read_b128 v[214:217], v192 offset:37376
	ds_read_b128 v[218:221], v192 offset:38912
	ds_read_b128 v[222:225], v192 offset:39424
	global_load_lds_dwordx4 v168, s[24:25]
	s_mov_b32 m0, s37
	s_nop 0
	global_load_lds_dwordx4 v164, s[24:25]
	s_waitcnt vmcnt(8)
	s_waitcnt lgkmcnt(0)
	s_barrier
	s_setprio 1
	s_waitcnt lgkmcnt(0)
	v_mfma_f32_16x16x128_f8f6f4 v[158:161], v[2:9], v[194:201], v[158:161]
	v_mfma_f32_16x16x128_f8f6f4 v[154:157], v[10:17], v[194:201], v[154:157]
	v_mfma_f32_16x16x128_f8f6f4 v[146:149], v[2:9], v[202:209], v[146:149]
	v_mfma_f32_16x16x128_f8f6f4 v[138:141], v[10:17], v[202:209], v[138:141]
	v_mfma_f32_16x16x128_f8f6f4 v[130:133], v[2:9], v[210:217], v[130:133]
	v_mfma_f32_16x16x128_f8f6f4 v[122:125], v[10:17], v[210:217], v[122:125]
	v_mfma_f32_16x16x128_f8f6f4 v[114:117], v[2:9], v[218:225], v[114:117]
	v_mfma_f32_16x16x128_f8f6f4 v[106:109], v[10:17], v[218:225], v[106:109]
	s_setprio 0
	s_setprio 1
	v_mfma_f32_16x16x128_f8f6f4 v[150:153], v[18:25], v[194:201], v[150:153]
	v_mfma_f32_16x16x128_f8f6f4 v[142:145], v[26:33], v[194:201], v[142:145]
	v_mfma_f32_16x16x128_f8f6f4 v[134:137], v[18:25], v[202:209], v[134:137]
	v_mfma_f32_16x16x128_f8f6f4 v[126:129], v[26:33], v[202:209], v[126:129]
	v_mfma_f32_16x16x128_f8f6f4 v[118:121], v[18:25], v[210:217], v[118:121]
	v_mfma_f32_16x16x128_f8f6f4 v[110:113], v[26:33], v[210:217], v[110:113]
	v_mfma_f32_16x16x128_f8f6f4 v[102:105], v[18:25], v[218:225], v[102:105]
	v_mfma_f32_16x16x128_f8f6f4 v[98:101], v[26:33], v[218:225], v[98:101]
	s_setprio 0
	s_barrier
	s_add_i32 s24, s53, s13
	s_add_i32 m0, s24, 0xffffff80
	ds_read_b128 v[194:197], v192 offset:49152
	ds_read_b128 v[198:201], v192 offset:49664
	ds_read_b128 v[202:205], v192 offset:51200
	ds_read_b128 v[206:209], v192 offset:51712
	ds_read_b128 v[210:213], v192 offset:53248
	ds_read_b128 v[214:217], v192 offset:53760
	ds_read_b128 v[218:221], v192 offset:55296
	ds_read_b128 v[222:225], v192 offset:55808
	global_load_lds_dwordx4 v166, s[28:29] offset:128
	s_add_i32 m0, s24, 0x2000
	s_add_u32 s24, s28, 0x80080
	v_lshl_add_u64 v[178:179], v[182:183], 0, s[8:9]
	s_addc_u32 s25, s29, 0
	s_add_i32 s28, s54, s13
	global_load_lds_dwordx4 v[178:179], off
	s_mov_b32 m0, s28
	s_nop 0
	global_load_lds_dwordx4 v166, s[24:25]
	s_add_i32 m0, s28, 0x2000
	s_nop 0
	global_load_lds_dwordx4 v162, s[24:25]
	s_add_i32 m0, s39, 0xffffff80
	s_nop 0
	global_load_lds_dwordx4 v168, s[30:31] offset:128
	s_add_i32 m0, s40, 0xffffff80
	s_nop 0
	global_load_lds_dwordx4 v164, s[30:31] offset:128
	s_waitcnt vmcnt(8)
	s_waitcnt lgkmcnt(0)
	s_barrier
	s_setprio 1
	s_waitcnt lgkmcnt(0)
	v_mfma_f32_16x16x128_f8f6f4 v[94:97], v[2:9], v[194:201], v[94:97]
	v_mfma_f32_16x16x128_f8f6f4 v[90:93], v[10:17], v[194:201], v[90:93]
	v_mfma_f32_16x16x128_f8f6f4 v[82:85], v[2:9], v[202:209], v[82:85]
	v_mfma_f32_16x16x128_f8f6f4 v[74:77], v[10:17], v[202:209], v[74:77]
	v_mfma_f32_16x16x128_f8f6f4 v[66:69], v[2:9], v[210:217], v[66:69]
	v_mfma_f32_16x16x128_f8f6f4 v[58:61], v[10:17], v[210:217], v[58:61]
	v_mfma_f32_16x16x128_f8f6f4 v[50:53], v[2:9], v[218:225], v[50:53]
	v_mfma_f32_16x16x128_f8f6f4 v[42:45], v[10:17], v[218:225], v[42:45]
	s_setprio 0
	s_setprio 1
	v_mfma_f32_16x16x128_f8f6f4 v[86:89], v[18:25], v[194:201], v[86:89]
	v_mfma_f32_16x16x128_f8f6f4 v[78:81], v[26:33], v[194:201], v[78:81]
	v_mfma_f32_16x16x128_f8f6f4 v[70:73], v[18:25], v[202:209], v[70:73]
	v_mfma_f32_16x16x128_f8f6f4 v[62:65], v[26:33], v[202:209], v[62:65]
	v_mfma_f32_16x16x128_f8f6f4 v[54:57], v[18:25], v[210:217], v[54:57]
	v_mfma_f32_16x16x128_f8f6f4 v[46:49], v[26:33], v[210:217], v[46:49]
	v_mfma_f32_16x16x128_f8f6f4 v[38:41], v[18:25], v[218:225], v[38:41]
	v_mfma_f32_16x16x128_f8f6f4 v[34:37], v[26:33], v[218:225], v[34:37]
	s_setprio 0
	s_barrier
	s_add_i32 s52, s52, 2
	s_add_u32 s50, s50, 0x100
	s_addc_u32 s51, s51, 0
	s_cmp_gt_u32 s52, 29
	s_mov_b64 s[24:25], s[26:27]
	s_cbranch_scc0 .LBB0_2358
	s_and_b64 vcc, exec, s[10:11]
	s_cbranch_vccz .LBB0_2361
	s_barrier

; #define PG8_STAGE(bufoff, gbase, voff) do { _Pragma("unroll") for (int _i = 0; _i < 2; ++_i) \
;         __builtin_amdgcn_global_load_lds((const unsigned*)((const char*)(gbase) + (voff)[_i]), (PG8_LAS unsigned*)(lds + (bufoff) + ldsw + _i * 8192), 16, 0, 0); } while (0)
; #define PG8_LDA(dst, b, h) do { _Pragma("unroll") for (int m = 0; m < 4; ++m) { const i32x4 _l = *(const PG8_LAS i32x4*)(lds + PG8_SA(b, h) + aoff + m * 2048), _h = *(const PG8_LAS i32x4*)(lds + PG8_SA(b, h) + aoff + m * 2048 + 512); dst[m] = PG8_CAT(_l, _h); } } while (0)
; #define PG8_LDB(dst, b, h) do { _Pragma("unroll") for (int n = 0; n < 2; ++n) { const i32x4 _l = *(const PG8_LAS i32x4*)(lds + PG8_SB(b, h) + boff + n * 2048), _h = *(const PG8_LAS i32x4*)(lds + PG8_SB(b, h) + boff + n * 2048 + 512); dst[n] = PG8_CAT(_l, _h); } } while (0)
; #define PG8_WAIT_V(n) asm volatile("s_waitcnt vmcnt(" #n ")" ::: "memory")
; #define PG8_WAIT_L(n) asm volatile("s_waitcnt lgkmcnt(" #n ")" ::: "memory")
; #define PG8_BAR __builtin_amdgcn_s_barrier()
; #define PG8_SCHED __builtin_amdgcn_sched_barrier(0)
;     ...
;         for (int t = 0; t < nt; t += 2) {
;             const bool last = (t == nt - 2);
;             const char* a1 = cA + (size_t)(t + 1) * kstep;
;             const char* a2 = last ? nA : cA + (size_t)(t + 2) * kstep; const char* b2 = last ? nB : cB + (size_t)(t + 2) * kstep;
;             const char* a3 = a2 + kstep; const char* b3 = b2 + kstep;
;             if (last && has_next) S.a_ready(nxt);
;             if constexpr (Epi::MIDK) { if (t == nt / 2) { if constexpr (ES == 1) asm volatile("s_nop 15\n\ts_nop 15" ::: "memory"); E.mid(acc, cur, wr, wc, fr, fq); } }
;             PG8_LDB(B0, 0, 0); PG8_LDB(B1, 0, 1); PG8_SCHED; PG8_LDA(At, 0, 0); PG8_STAGE(PG8_SA(1, 1), a1 + hstepA, voffA);
;             PG8_WAIT_V(8); PG8_WAIT_L(0); PG8_BAR; PG8_MMA(0, 0, At, B0); PG8_MMA(0, 1, At, B1); PG8_BAR; PG8_SCHED;
;             PG8_LDA(At, 0, 1); PG8_STAGE(PG8_SB(0, 0), b2, voffB); PG8_STAGE(PG8_SB(0, 1), b2 + hstepB, voffB); PG8_STAGE(PG8_SA(0, 0), a2, voffA);
;             PG8_WAIT_V(8); PG8_WAIT_L(0); PG8_BAR; PG8_MMA(1, 0, At, B0); PG8_MMA(1, 1, At, B1); PG8_BAR; PG8_SCHED;
.LBB0_2648:
	ds_read_b128 v[16:19], v183
	ds_read_b128 v[20:23], v183 offset:512
	ds_read_b128 v[24:27], v183 offset:2048
	ds_read_b128 v[28:31], v183 offset:2560
	ds_read_b128 v[0:3], v184
	ds_read_b128 v[4:7], v184 offset:512
	ds_read_b128 v[8:11], v184 offset:2048
	ds_read_b128 v[12:15], v184 offset:2560
	s_add_u32 s46, s44, 0x100
	s_addc_u32 s47, s45, 0
	s_cmpk_eq_i32 s83, 0x52
	s_cselect_b32 s51, s3, s47
	s_cselect_b32 s50, s2, s46
	s_cselect_b32 s49, s43, s82
	s_cselect_b32 s48, s42, s81
	s_add_i32 m0, s52, 0xc000
	ds_read_b128 v[172:175], v185
	ds_read_b128 v[176:179], v185 offset:512
	ds_read_b128 v[186:189], v185 offset:2048
	ds_read_b128 v[190:193], v185 offset:2560
	ds_read_b128 v[194:197], v185 offset:4096
	ds_read_b128 v[198:201], v185 offset:4608
	ds_read_b128 v[202:205], v185 offset:6144
	ds_read_b128 v[206:209], v185 offset:6656
	global_load_lds_dwordx4 v164, s[44:45]
	s_add_i32 m0, s52, 0xe000
	s_nop 0
	global_load_lds_dwordx4 v166, s[44:45]
	s_waitcnt vmcnt(8)
	s_waitcnt lgkmcnt(0)
	s_barrier
	s_setprio 1
	s_waitcnt lgkmcnt(0)
	v_mfma_f32_16x16x128_f8f6f4 v[156:159], v[16:23], v[172:179], v[156:159]
	v_mfma_f32_16x16x128_f8f6f4 v[152:155], v[24:31], v[172:179], v[152:155]
	v_mfma_f32_16x16x128_f8f6f4 v[140:143], v[16:23], v[186:193], v[140:143]
	v_mfma_f32_16x16x128_f8f6f4 v[136:139], v[24:31], v[186:193], v[136:139]
	v_mfma_f32_16x16x128_f8f6f4 v[124:127], v[16:23], v[194:201], v[124:127]
	v_mfma_f32_16x16x128_f8f6f4 v[120:123], v[24:31], v[194:201], v[120:123]
	v_mfma_f32_16x16x128_f8f6f4 v[108:111], v[16:23], v[202:209], v[108:111]
	v_mfma_f32_16x16x128_f8f6f4 v[104:107], v[24:31], v[202:209], v[104:107]
	s_setprio 0
	s_setprio 1
	v_mfma_f32_16x16x128_f8f6f4 v[148:151], v[0:7], v[172:179], v[148:151]
	v_mfma_f32_16x16x128_f8f6f4 v[144:147], v[8:15], v[172:179], v[144:147]
	v_mfma_f32_16x16x128_f8f6f4 v[132:135], v[0:7], v[186:193], v[132:135]
	v_mfma_f32_16x16x128_f8f6f4 v[128:131], v[8:15], v[186:193], v[128:131]
	v_mfma_f32_16x16x128_f8f6f4 v[116:119], v[0:7], v[194:201], v[116:119]
	v_mfma_f32_16x16x128_f8f6f4 v[112:115], v[8:15], v[194:201], v[112:115]
	v_mfma_f32_16x16x128_f8f6f4 v[100:103], v[0:7], v[202:209], v[100:103]
	v_mfma_f32_16x16x128_f8f6f4 v[96:99], v[8:15], v[202:209], v[96:99]
	s_setprio 0
	s_barrier
	s_add_i32 s44, s62, s33
	s_mov_b32 m0, s44
	ds_read_b128 v[186:189], v185 offset:16384
	ds_read_b128 v[190:193], v185 offset:16896
	ds_read_b128 v[194:197], v185 offset:18432
	ds_read_b128 v[198:201], v185 offset:18944
	ds_read_b128 v[202:205], v185 offset:20480
	ds_read_b128 v[206:209], v185 offset:20992
	ds_read_b128 v[210:213], v185 offset:22528
	ds_read_b128 v[214:217], v185 offset:23040
	global_load_lds_dwordx4 v160, s[48:49]
	s_add_i32 m0, s44, 0x2000
	s_add_u32 s44, s48, 0x158000
	v_lshl_add_u64 v[174:175], s[48:49], 0, v[162:163]
	s_addc_u32 s45, s49, 0
	s_add_i32 s84, s63, s33
	global_load_lds_dwordx4 v162, s[48:49]
	s_mov_b32 m0, s84
	s_nop 0
	global_load_lds_dwordx4 v160, s[44:45]
	s_add_i32 m0, s84, 0x2000
	s_nop 0
	global_load_lds_dwordx4 v162, s[44:45]
	s_mov_b32 m0, s52
	s_nop 0
	global_load_lds_dwordx4 v160, s[50:51]
	s_mov_b32 m0, s53
	s_nop 0
	global_load_lds_dwordx4 v162, s[50:51]
	s_waitcnt vmcnt(8)
	s_waitcnt lgkmcnt(0)
	s_barrier
	s_setprio 1
	s_waitcnt lgkmcnt(0)
	v_mfma_f32_16x16x128_f8f6f4 v[92:95], v[16:23], v[186:193], v[92:95]
	v_mfma_f32_16x16x128_f8f6f4 v[88:91], v[24:31], v[186:193], v[88:91]
	v_mfma_f32_16x16x128_f8f6f4 v[76:79], v[16:23], v[194:201], v[76:79]
	v_mfma_f32_16x16x128_f8f6f4 v[72:75], v[24:31], v[194:201], v[72:75]
	v_mfma_f32_16x16x128_f8f6f4 v[60:63], v[16:23], v[202:209], v[60:63]
	v_mfma_f32_16x16x128_f8f6f4 v[56:59], v[24:31], v[202:209], v[56:59]
	v_mfma_f32_16x16x128_f8f6f4 v[52:55], v[16:23], v[210:217], v[52:55]
	v_mfma_f32_16x16x128_f8f6f4 v[44:47], v[24:31], v[210:217], v[44:47]
	s_setprio 0
	s_setprio 1
	v_mfma_f32_16x16x128_f8f6f4 v[84:87], v[0:7], v[186:193], v[84:87]
	v_mfma_f32_16x16x128_f8f6f4 v[80:83], v[8:15], v[186:193], v[80:83]
	v_mfma_f32_16x16x128_f8f6f4 v[68:71], v[0:7], v[194:201], v[68:71]
	v_mfma_f32_16x16x128_f8f6f4 v[64:67], v[8:15], v[194:201], v[64:67]
	v_mfma_f32_16x16x128_f8f6f4 v[48:51], v[0:7], v[202:209], v[48:51]
	v_mfma_f32_16x16x128_f8f6f4 v[40:43], v[8:15], v[202:209], v[40:43]
	v_mfma_f32_16x16x128_f8f6f4 v[36:39], v[0:7], v[210:217], v[36:39]
	v_mfma_f32_16x16x128_f8f6f4 v[32:35], v[8:15], v[210:217], v[32:35]
	s_setprio 0
	s_barrier
; #define PG8_STAGE(bufoff, gbase, voff) do { _Pragma("unroll") for (int _i = 0; _i < 2; ++_i) \
;         __builtin_amdgcn_global_load_lds((const unsigned*)((const char*)(gbase) + (voff)[_i]), (PG8_LAS unsigned*)(lds + (bufoff) + ldsw + _i * 8192), 16, 0, 0); } while (0)
; #define PG8_LDA(dst, b, h) do { _Pragma("unroll") for (int m = 0; m < 4; ++m) { const i32x4 _l = *(const PG8_LAS i32x4*)(lds + PG8_SA(b, h) + aoff + m * 2048), _h = *(const PG8_LAS i32x4*)(lds + PG8_SA(b, h) + aoff + m * 2048 + 512); dst[m] = PG8_CAT(_l, _h); } } while (0)
; #define PG8_LDB(dst, b, h) do { _Pragma("unroll") for (int n = 0; n < 2; ++n) { const i32x4 _l = *(const PG8_LAS i32x4*)(lds + PG8_SB(b, h) + boff + n * 2048), _h = *(const PG8_LAS i32x4*)(lds + PG8_SB(b, h) + boff + n * 2048 + 512); dst[n] = PG8_CAT(_l, _h); } } while (0)
; #define PG8_WAIT_V(n) asm volatile("s_waitcnt vmcnt(" #n ")" ::: "memory")
; #define PG8_WAIT_L(n) asm volatile("s_waitcnt lgkmcnt(" #n ")" ::: "memory")
; #define PG8_BAR __builtin_amdgcn_s_barrier()
; #define PG8_SCHED __builtin_amdgcn_sched_barrier(0)
;     ...
;             PG8_LDB(B0, 1, 0); PG8_LDB(B1, 1, 1); PG8_SCHED; PG8_LDA(At, 1, 0); PG8_STAGE(PG8_SA(0, 1), a2 + hstepA, voffA);
;             PG8_WAIT_V(8); PG8_WAIT_L(0); PG8_BAR; PG8_MMA(0, 0, At, B0); PG8_MMA(0, 1, At, B1); PG8_BAR; PG8_SCHED;
;             PG8_LDA(At, 1, 1); PG8_STAGE(PG8_SB(1, 0), b3, voffB); PG8_STAGE(PG8_SB(1, 1), b3 + hstepB, voffB); PG8_STAGE(PG8_SA(1, 0), a3, voffA);
;             PG8_WAIT_V(8); PG8_WAIT_L(0); PG8_BAR; PG8_MMA(1, 0, At, B0); PG8_MMA(1, 1, At, B1); PG8_BAR; PG8_SCHED;
;         }
	s_add_i32 s84, 0, 0x18000
	s_add_i32 s85, 0, 0x1c000
	v_add_u32_e32 v12, s84, v181
	v_add_u32_e32 v28, s85, v181
	ds_read_b128 v[0:3], v12
	ds_read_b128 v[4:7], v12 offset:512
	ds_read_b128 v[8:11], v12 offset:2048
	ds_read_b128 v[12:15], v12 offset:2560
	ds_read_b128 v[16:19], v28
	ds_read_b128 v[20:23], v28 offset:512
	ds_read_b128 v[24:27], v28 offset:2048
	ds_read_b128 v[28:31], v28 offset:2560
	s_add_u32 s44, s50, 0x158000
	s_addc_u32 s45, s51, 0
	s_mov_b32 m0, s54
	ds_read_b128 v[186:189], v185 offset:32768
	ds_read_b128 v[190:193], v185 offset:33280
	ds_read_b128 v[194:197], v185 offset:34816
	ds_read_b128 v[198:201], v185 offset:35328
	ds_read_b128 v[202:205], v185 offset:36864
	ds_read_b128 v[206:209], v185 offset:37376
	ds_read_b128 v[210:213], v185 offset:38912
	ds_read_b128 v[214:217], v185 offset:39424
	global_load_lds_dwordx4 v160, s[44:45]
	s_mov_b32 m0, s55
	s_nop 0
	global_load_lds_dwordx4 v162, s[44:45]
	s_waitcnt vmcnt(8)
	s_waitcnt lgkmcnt(0)
	s_barrier
	s_setprio 1
	s_waitcnt lgkmcnt(0)
	v_mfma_f32_16x16x128_f8f6f4 v[156:159], v[0:7], v[186:193], v[156:159]
	v_mfma_f32_16x16x128_f8f6f4 v[152:155], v[8:15], v[186:193], v[152:155]
	v_mfma_f32_16x16x128_f8f6f4 v[140:143], v[0:7], v[194:201], v[140:143]
	v_mfma_f32_16x16x128_f8f6f4 v[136:139], v[8:15], v[194:201], v[136:139]
	v_mfma_f32_16x16x128_f8f6f4 v[124:127], v[0:7], v[202:209], v[124:127]
	v_mfma_f32_16x16x128_f8f6f4 v[120:123], v[8:15], v[202:209], v[120:123]
	v_mfma_f32_16x16x128_f8f6f4 v[108:111], v[0:7], v[210:217], v[108:111]
	v_mfma_f32_16x16x128_f8f6f4 v[104:107], v[8:15], v[210:217], v[104:107]
	s_setprio 0
	s_setprio 1
	v_mfma_f32_16x16x128_f8f6f4 v[148:151], v[16:23], v[186:193], v[148:151]
	v_mfma_f32_16x16x128_f8f6f4 v[144:147], v[24:31], v[186:193], v[144:147]
	v_mfma_f32_16x16x128_f8f6f4 v[132:135], v[16:23], v[194:201], v[132:135]
	v_mfma_f32_16x16x128_f8f6f4 v[128:131], v[24:31], v[194:201], v[128:131]
	v_mfma_f32_16x16x128_f8f6f4 v[116:119], v[16:23], v[202:209], v[116:119]
	v_mfma_f32_16x16x128_f8f6f4 v[112:115], v[24:31], v[202:209], v[112:115]
	v_mfma_f32_16x16x128_f8f6f4 v[100:103], v[16:23], v[210:217], v[100:103]
	v_mfma_f32_16x16x128_f8f6f4 v[96:99], v[24:31], v[210:217], v[96:99]
	s_setprio 0
	s_barrier
	s_add_i32 s44, s84, s33
	s_add_i32 m0, s44, 0xffffff80
	ds_read_b128 v[186:189], v185 offset:49152
	ds_read_b128 v[190:193], v185 offset:49664
	ds_read_b128 v[194:197], v185 offset:51200
	ds_read_b128 v[198:201], v185 offset:51712
	ds_read_b128 v[202:205], v185 offset:53248
	ds_read_b128 v[206:209], v185 offset:53760
	ds_read_b128 v[210:213], v185 offset:55296
	ds_read_b128 v[214:217], v185 offset:55808
	global_load_lds_dwordx4 v160, s[48:49] offset:128
	s_add_i32 m0, s44, 0x2000
	s_add_u32 s44, s48, 0x158080
	v_lshl_add_u64 v[172:173], v[174:175], 0, s[8:9]
	s_addc_u32 s45, s49, 0
	s_add_i32 s48, s85, s33
	global_load_lds_dwordx4 v[172:173], off
	s_mov_b32 m0, s48
	s_nop 0
	global_load_lds_dwordx4 v160, s[44:45]
	s_add_i32 m0, s48, 0x2000
	s_nop 0
	global_load_lds_dwordx4 v162, s[44:45]
	s_add_i32 m0, s59, 0xffffff80
	s_nop 0
	global_load_lds_dwordx4 v160, s[50:51] offset:128
	s_add_i32 m0, s60, 0xffffff80
	s_nop 0
	global_load_lds_dwordx4 v162, s[50:51] offset:128
	s_waitcnt vmcnt(8)
	s_waitcnt lgkmcnt(0)
	s_barrier
	s_setprio 1
	s_waitcnt lgkmcnt(0)
	v_mfma_f32_16x16x128_f8f6f4 v[92:95], v[0:7], v[186:193], v[92:95]
	v_mfma_f32_16x16x128_f8f6f4 v[88:91], v[8:15], v[186:193], v[88:91]
	v_mfma_f32_16x16x128_f8f6f4 v[76:79], v[0:7], v[194:201], v[76:79]
	v_mfma_f32_16x16x128_f8f6f4 v[72:75], v[8:15], v[194:201], v[72:75]
	v_mfma_f32_16x16x128_f8f6f4 v[60:63], v[0:7], v[202:209], v[60:63]
	v_mfma_f32_16x16x128_f8f6f4 v[56:59], v[8:15], v[202:209], v[56:59]
	v_mfma_f32_16x16x128_f8f6f4 v[52:55], v[0:7], v[210:217], v[52:55]
	v_mfma_f32_16x16x128_f8f6f4 v[44:47], v[8:15], v[210:217], v[44:47]
	s_setprio 0
	s_setprio 1
	v_mfma_f32_16x16x128_f8f6f4 v[84:87], v[16:23], v[186:193], v[84:87]
	v_mfma_f32_16x16x128_f8f6f4 v[80:83], v[24:31], v[186:193], v[80:83]
	v_mfma_f32_16x16x128_f8f6f4 v[68:71], v[16:23], v[194:201], v[68:71]
	v_mfma_f32_16x16x128_f8f6f4 v[64:67], v[24:31], v[194:201], v[64:67]
	v_mfma_f32_16x16x128_f8f6f4 v[48:51], v[16:23], v[202:209], v[48:51]
	v_mfma_f32_16x16x128_f8f6f4 v[40:43], v[24:31], v[202:209], v[40:43]
	v_mfma_f32_16x16x128_f8f6f4 v[36:39], v[16:23], v[210:217], v[36:39]
	v_mfma_f32_16x16x128_f8f6f4 v[32:35], v[24:31], v[210:217], v[32:35]
	s_setprio 0
	s_barrier
	s_add_i32 s83, s83, 2
	s_add_u32 s81, s81, 0x100
	s_addc_u32 s82, s82, 0
	s_cmpk_gt_u32 s83, 0x53
	s_mov_b64 s[44:45], s[46:47]
	s_cbranch_scc0 .LBB0_2648
	s_and_b64 vcc, exec, s[10:11]
	s_cbranch_vccz .LBB0_2651
	s_barrier
